# router: norm gain folded into the split-bf16 router weights in phase 0 (activation operand = bf16 h itself, 2 MFMAs per fragment, no per-token conversion), row sum of squares from an h*h^T MFMA diagon
# speedup vs baseline: 1.0770x; 1.0003x over previous
; __device__ __forceinline__ unsigned f2bf(float f) { unsigned u = __builtin_bit_cast(unsigned, f); return (u + 0x7fffu + ((u >> 16) & 1u)) >> 16; }
; __device__ __forceinline__ void p0_prologue(Frame& F) {
;     ...
;     { bf16_t* RBH = (bf16_t*)(F.ws + WS_RB); bf16_t* RBL = RBH + 80 * D;
;       for (int i = F.bid * NTHREADS + F.tid; i < 80 * D; i += F.G * NTHREADS) { const int c = i / D, k = i % D;
;           float v = 0.f; if (c < 8) v = F.rg_w[k * 8 + c]; else if (c < 72) { const int g = (c - 8) >> 3, j = (c - 8) & 7; v = F.re_w[((size_t)g * D + k) * 8 + j]; }
;           const unsigned h = f2bf(v); const float hf = __builtin_bit_cast(float, h << 16); RBH[i] = (bf16_t)h; RBL[i] = (bf16_t)f2bf(v - hf); } }
.LBB0_112:
	s_or_b64 exec, exec, s[0:1]
	v_add_u32_e32 v2, s13, v0
	s_mov_b32 s0, 0x50000
	v_cmp_gt_i32_e32 vcc, s0, v2
	s_and_saveexec_b64 s[0:1], vcc
	s_cbranch_execz .LBB0_121
	v_readlane_b32 s98, v254, 9
	v_readlane_b32 s99, v254, 10
	v_readlane_b32 s20, v254, 25
	v_readlane_b32 s26, v254, 31
	v_readlane_b32 s27, v254, 32
	s_add_u32 s4, s26, 0xe00000
	s_addc_u32 s5, s27, 0
	s_add_u32 s6, s26, 0xea0000
	s_addc_u32 s7, s27, 0
	v_lshl_or_b32 v3, s2, 12, v154
	s_lshl_b32 s3, s16, 3
	s_mov_b64 s[8:9], 0
	s_movk_i32 s13, 0x7fff
	s_mov_b32 s15, 0x48000
	v_mov_b32_e32 v5, 0
	s_mov_b32 s17, 0x4ffff
	v_mov_b32_e32 v6, v2
	v_readlane_b32 s21, v254, 26
	v_readlane_b32 s22, v254, 27
	v_readlane_b32 s23, v254, 28
	v_readlane_b32 s24, v254, 29
	v_readlane_b32 s25, v254, 30
	s_branch .LBB0_115
.LBB0_114:
	s_or_b64 exec, exec, s[18:19]
	s_waitcnt vmcnt(0)
	v_mul_f32_e32 v4, v4, v180
	v_bfe_u32 v8, v4, 16, 1
	v_add3_u32 v12, v4, v8, s13
	v_and_b32_e32 v13, 0xffff0000, v12
	v_lshlrev_b64 v[8:9], 1, v[6:7]
	v_sub_f32_e32 v4, v4, v13
	v_add_u32_e32 v6, s16, v6
	v_bfe_u32 v7, v4, 16, 1
	v_cmp_lt_i32_e32 vcc, s17, v6
	v_lshl_add_u64 v[10:11], s[4:5], 0, v[8:9]
	v_add3_u32 v4, v4, v7, s13
	v_lshl_add_u64 v[8:9], s[6:7], 0, v[8:9]
	s_or_b64 s[8:9], vcc, s[8:9]
	v_add_u32_e32 v3, s3, v3
	global_store_short_d16_hi v[10:11], v12, off
	global_store_short_d16_hi v[8:9], v4, off
	s_andn2_b64 exec, exec, s[8:9]
	s_cbranch_execz .LBB0_121
.LBB0_115:
	v_and_b32_e32 v181, 0xfff, v6
	v_lshlrev_b32_e32 v181, 2, v181
	global_load_dword v180, v181, s[98:99]
	v_ashrrev_i32_e32 v7, 31, v6
	v_lshrrev_b32_e32 v4, 20, v7
	v_add_u32_e32 v4, v6, v4
	v_ashrrev_i32_e32 v9, 12, v4
	v_mul_i32_i24_e32 v8, 0x1000, v9
	v_cmp_lt_i32_e32 vcc, s13, v6
	s_and_saveexec_b64 s[18:19], vcc
	s_xor_b64 s[18:19], exec, s[18:19]
	s_cbranch_execz .LBB0_119
	v_cmp_gt_u32_e32 vcc, s15, v6
	v_mov_b32_e32 v4, 0
	s_and_saveexec_b64 s[20:21], vcc
	s_cbranch_execz .LBB0_118
	v_add_u32_e32 v4, -8, v9
	v_lshrrev_b32_e32 v4, 3, v4
	v_readlane_b32 s36, v254, 7
	v_lshlrev_b32_e32 v8, 3, v8
	v_lshlrev_b64 v[10:11], 17, v[4:5]
	v_readlane_b32 s44, v254, 15
	v_readlane_b32 s45, v254, 16
	v_and_b32_e32 v12, 7, v9
	v_sub_u32_e32 v8, v3, v8
	v_mov_b32_e32 v9, v5
	v_lshl_add_u64 v[10:11], s[44:45], 0, v[10:11]
	v_lshl_add_u64 v[8:9], v[8:9], 2, v[10:11]
	v_lshlrev_b32_e32 v4, 2, v12
	v_lshl_add_u64 v[8:9], v[8:9], 0, v[4:5]
	global_load_dword v4, v[8:9], off
	v_readlane_b32 s37, v254, 8
	v_readlane_b32 s38, v254, 9
	v_readlane_b32 s39, v254, 10
	v_readlane_b32 s40, v254, 11
	v_readlane_b32 s41, v254, 12
	v_readlane_b32 s42, v254, 13
	v_readlane_b32 s43, v254, 14
	v_readlane_b32 s46, v254, 17
	v_readlane_b32 s47, v254, 18
	v_readlane_b32 s48, v254, 19
	v_readlane_b32 s49, v254, 20
	v_readlane_b32 s50, v254, 21
	v_readlane_b32 s51, v254, 22

; __device__ __forceinline__ void p5_router(Frame& F) {
;     ...
;           const size_t roff = (size_t)(m0 + 32 * tg + fr) * D + kq * 1024 + 8 * fq;
;           const bf16_t* h0 = H + roff; const bf16_t* h1 = h0 + (size_t)16 * D;
;           const float* gp = F.g_ffn + kq * 1024 + 8 * fq;
;           const bf16_t* bh = RBH + (size_t)fr * D + kq * 1024 + 8 * fq; const bf16_t* bl = RBL + (size_t)fr * D + kq * 1024 + 8 * fq;
;           RtLoad La, Lb; rt_load(La, h0, h1, gp, 0);
.LBB0_606:
	s_lshl_b32 s10, s64, 6
	v_readlane_b32 s84, v254, 23
	v_readlane_b32 s86, v254, 31
	v_readlane_b32 s87, v254, 32
	s_and_b32 s88, s84, 3
	s_lshr_b32 s89, s84, 2
	s_mov_b32 s94, 0xe00000
	s_mov_b32 s95, 0xea0000
	s_lshl_b32 s91, s64, 19
	s_add_i32 s91, s91, 0x29e00000
	v_and_b32_e32 v217, 7, v131
	v_lshrrev_b32_e32 v218, 1, v130
	v_lshlrev_b32_e32 v219, 13, v130
	s_add_i32 s24, s84, 0
	s_lshl_b32 s98, s24, 10
	s_sub_i32 s85, s24, 10
	s_sub_i32 s33, s24, 20
	s_cmp_lt_u32 s24, 20
	s_cselect_b32 s33, s85, s33
	s_cselect_b32 s85, s95, s91
	s_cmp_lt_u32 s24, 10
	s_cselect_b32 s33, s24, s33
	s_cselect_b32 s85, s94, s85
	s_and_b32 s24, s33, 1
	s_lshl_b32 s24, s24, 2
	s_lshl_b32 s33, s33, 16
	s_add_i32 s85, s85, s33
	v_add_u32_e32 v220, s24, v218
	v_xor_b32_e32 v220, v220, v217
	v_lshl_add_u32 v220, v220, 4, v219
	v_add_u32_e32 v208, s85, v220
	s_add_i32 s24, s84, 8
	s_lshl_b32 s99, s24, 10
	s_sub_i32 s85, s24, 10
	s_sub_i32 s33, s24, 20
	s_cmp_lt_u32 s24, 20
	s_cselect_b32 s33, s85, s33
	s_cselect_b32 s85, s95, s91
	s_cmp_lt_u32 s24, 10
	s_cselect_b32 s33, s24, s33
	s_cselect_b32 s85, s94, s85
	s_and_b32 s24, s33, 1
	s_lshl_b32 s24, s24, 2
	s_lshl_b32 s33, s33, 16
	s_add_i32 s85, s85, s33
	v_add_u32_e32 v220, s24, v218
	v_xor_b32_e32 v220, v220, v217
	v_lshl_add_u32 v220, v220, 4, v219
	v_add_u32_e32 v209, s85, v220
	s_add_i32 s24, s84, 16
	s_lshl_b32 s100, s24, 10
	s_sub_i32 s85, s24, 10
	s_sub_i32 s33, s24, 20
	s_cmp_lt_u32 s24, 20
	s_cselect_b32 s33, s85, s33
	s_cselect_b32 s85, s95, s91
	s_cmp_lt_u32 s24, 10
	s_cselect_b32 s33, s24, s33
	s_cselect_b32 s85, s94, s85
	s_and_b32 s24, s33, 1
	s_lshl_b32 s24, s24, 2
	s_lshl_b32 s33, s33, 16
	s_add_i32 s85, s85, s33
	v_add_u32_e32 v220, s24, v218
	v_xor_b32_e32 v220, v220, v217
	v_lshl_add_u32 v220, v220, 4, v219
	v_add_u32_e32 v210, s85, v220
	s_add_i32 s24, s84, 24
	s_lshl_b32 s101, s24, 10
	s_sub_i32 s85, s24, 10
	s_sub_i32 s33, s24, 20
	s_cmp_lt_u32 s24, 20
	s_cselect_b32 s33, s85, s33
	s_cselect_b32 s85, s95, s91
	s_cmp_lt_u32 s24, 10
	s_cselect_b32 s33, s24, s33
	s_cselect_b32 s85, s94, s85
	s_and_b32 s24, s33, 1
	s_lshl_b32 s24, s24, 2
	s_lshl_b32 s33, s33, 16
	s_add_i32 s85, s85, s33
	v_add_u32_e32 v220, s24, v218
	v_xor_b32_e32 v220, v220, v217
	v_lshl_add_u32 v220, v220, 4, v219
	v_add_u32_e32 v211, s85, v220
	s_lshl_b32 s24, s89, 2
	v_add_u32_e32 v217, s24, v171
	v_bfe_u32 v218, v131, 1, 3
	v_xor_b32_e32 v217, v217, v218
	v_lshlrev_b32_e32 v217, 4, v217
	v_lshl_add_u32 v212, v170, 7, v217
	s_lshl_b32 s24, s88, 11
	s_add_i32 s24, s24, 20480
	v_add_u32_e32 v213, s24, v212
	s_lshr_b32 s39, s64, 2
	s_and_b32 s39, s39, 62
	s_lshl_b32 s39, s39, 7
	s_sub_u32 s39, s39, 0x80
	s_cmp_gt_u32 s84, 3
	s_cbranch_scc1 .Lrt_pro3
	s_add_i32 s39, s39, 0x80
	s_and_b32 s39, s39, 0x1fff
	s_add_u32 s40, s86, s39
	s_addc_u32 s41, s87, 0
	s_mov_b32 m0, s98
	s_nop 0
	global_load_lds_dwordx4 v208, s[40:41]
	s_mov_b32 m0, s99
	s_nop 0
	global_load_lds_dwordx4 v209, s[40:41]
	s_mov_b32 m0, s100
	s_nop 0
	global_load_lds_dwordx4 v210, s[40:41]
	s_mov_b32 m0, s101
	s_nop 0
	global_load_lds_dwordx4 v211, s[40:41]
	s_add_i32 s39, s39, 0x80
	s_and_b32 s39, s39, 0x1fff
	s_add_u32 s40, s86, s39
	s_addc_u32 s41, s87, 0
	s_add_i32 m0, s98, 28672
	s_nop 0
	global_load_lds_dwordx4 v208, s[40:41]
	s_add_i32 m0, s99, 28672
	s_nop 0
	global_load_lds_dwordx4 v209, s[40:41]
	s_add_i32 m0, s100, 28672
	s_nop 0
	global_load_lds_dwordx4 v210, s[40:41]
	s_add_i32 m0, s101, 28672
	s_nop 0
	global_load_lds_dwordx4 v211, s[40:41]
	s_add_i32 s39, s39, 0x80
	s_and_b32 s39, s39, 0x1fff
	s_add_u32 s40, s86, s39
	s_addc_u32 s41, s87, 0
	s_add_i32 m0, s98, 57344
	s_nop 0
	global_load_lds_dwordx4 v208, s[40:41]
	s_add_i32 m0, s99, 57344
	s_nop 0
	global_load_lds_dwordx4 v209, s[40:41]
	s_add_i32 m0, s100, 57344
	s_nop 0
	global_load_lds_dwordx4 v210, s[40:41]
	s_add_i32 m0, s101, 57344
	s_nop 0
	global_load_lds_dwordx4 v211, s[40:41]
	s_waitcnt vmcnt(8)
	s_branch .Lrt_prodone
.Lrt_pro3:
	s_add_i32 s39, s39, 0x80
	s_and_b32 s39, s39, 0x1fff
	s_add_u32 s40, s86, s39
	s_addc_u32 s41, s87, 0
	s_mov_b32 m0, s98
	s_nop 0
	global_load_lds_dwordx4 v208, s[40:41]
	s_mov_b32 m0, s99
	s_nop 0
	global_load_lds_dwordx4 v209, s[40:41]
	s_mov_b32 m0, s100
	s_nop 0
	global_load_lds_dwordx4 v210, s[40:41]
	s_add_i32 s39, s39, 0x80
	s_and_b32 s39, s39, 0x1fff
	s_add_u32 s40, s86, s39
	s_addc_u32 s41, s87, 0
	s_add_i32 m0, s98, 28672
	s_nop 0
	global_load_lds_dwordx4 v208, s[40:41]
	s_add_i32 m0, s99, 28672
	s_nop 0
	global_load_lds_dwordx4 v209, s[40:41]
	s_add_i32 m0, s100, 28672
	s_nop 0
	global_load_lds_dwordx4 v210, s[40:41]
	s_add_i32 s39, s39, 0x80
	s_and_b32 s39, s39, 0x1fff
	s_add_u32 s40, s86, s39
	s_addc_u32 s41, s87, 0
	s_add_i32 m0, s98, 57344
	s_nop 0
	global_load_lds_dwordx4 v208, s[40:41]
	s_add_i32 m0, s99, 57344
	s_nop 0
	global_load_lds_dwordx4 v209, s[40:41]
	s_add_i32 m0, s100, 57344
	s_nop 0
	global_load_lds_dwordx4 v210, s[40:41]
	s_waitcnt vmcnt(6)
; __device__ __forceinline__ void rt_step(const RtLoad& L, const bf16_t* bh, const bf16_t* bl, f32x4 (&acc)[2][5], float (&ss)[2], int ko) {
;     RtW W;
; #pragma unroll
;     for (int n = 0; n < 5; ++n) { W.wh[n] = *(const bf16x8*)(bh + (size_t)n * 16 * D + ko); W.wl[n] = *(const bf16x8*)(bl + (size_t)n * 16 * D + ko); }
;     bf16x8 ahi[2], alo[2];
; #pragma unroll
;     for (int mi = 0; mi < 2; ++mi) { const u32x4 xw = L.x[mi]; const f32x4 xa = (f32x4){bflo(xw.x), bfhi(xw.x), bflo(xw.y), bfhi(xw.y)}, xb = (f32x4){bflo(xw.z), bfhi(xw.z), bflo(xw.w), bfhi(xw.w)};
;         ss[mi] += (xa.x * xa.x + xa.y * xa.y) + (xa.z * xa.z + xa.w * xa.w) + (xb.x * xb.x + xb.y * xb.y) + (xb.z * xb.z + xb.w * xb.w);
;         const float u[8] = {xa.x * L.g[0].x, xa.y * L.g[0].y, xa.z * L.g[0].z, xa.w * L.g[0].w, xb.x * L.g[1].x, xb.y * L.g[1].y, xb.z * L.g[1].z, xb.w * L.g[1].w};
;         unsigned hb[8]; float lo[8];
; #pragma unroll
;         for (int j = 0; j < 8; ++j) { hb[j] = f2bf(u[j]); lo[j] = u[j] - __builtin_bit_cast(float, hb[j] << 16); }
;         const u32x4 hw = (u32x4){hb[0] | (hb[1] << 16), hb[2] | (hb[3] << 16), hb[4] | (hb[5] << 16), hb[6] | (hb[7] << 16)};
;         const u32x4 lw = (u32x4){pk2(lo[0], lo[1]), pk2(lo[2], lo[3]), pk2(lo[4], lo[5]), pk2(lo[6], lo[7])};
; __device__ __forceinline__ void p5_router(Frame& F) {
;     ...
;         { const int tg = wave & 1, kq = wave >> 1, fr = lane & 15, fq = lane >> 4;
;           f32x4 acc[2][5];
; #pragma unroll
;           for (int a = 0; a < 2; ++a)
; #pragma unroll
;               for (int n = 0; n < 5; ++n) acc[a][n] = (f32x4){0.f, 0.f, 0.f, 0.f};
;           float ss[2] = {0.f, 0.f};
;           const size_t roff = (size_t)(m0 + 32 * tg + fr) * D + kq * 1024 + 8 * fq;
;           const bf16_t* h0 = H + roff; const bf16_t* h1 = h0 + (size_t)16 * D;
;           const float* gp = F.g_ffn + kq * 1024 + 8 * fq;
;           const bf16_t* bh = RBH + (size_t)fr * D + kq * 1024 + 8 * fq; const bf16_t* bl = RBL + (size_t)fr * D + kq * 1024 + 8 * fq;
;           RtLoad La, Lb; rt_load(La, h0, h1, gp, 0);
; #pragma unroll 1
;           for (int ks = 0; ks < 32; ks += 2) {
;               rt_load(Lb, h0, h1, gp, (ks + 1) * 32); rt_step(La, bh, bl, acc, ss, ks * 32);
;               if (ks + 2 < 32) rt_load(La, h0, h1, gp, (ks + 2) * 32);
;               rt_step(Lb, bh, bl, acc, ss, (ks + 1) * 32); }
.Lrt_prodone:
	v_mov_b32_e32 v18, 0
	v_mov_b32_e32 v19, 0
	v_mov_b32_e32 v20, 0
	v_mov_b32_e32 v21, 0
	v_mov_b32_e32 v22, 0
	v_mov_b32_e32 v23, 0
	v_mov_b32_e32 v24, 0
	v_mov_b32_e32 v25, 0
	v_mov_b32_e32 v26, 0
	v_mov_b32_e32 v27, 0
	v_mov_b32_e32 v28, 0
	v_mov_b32_e32 v29, 0
	v_mov_b32_e32 v30, 0
	v_mov_b32_e32 v31, 0
	v_mov_b32_e32 v32, 0
	v_mov_b32_e32 v33, 0
	v_mov_b32_e32 v34, 0
	v_mov_b32_e32 v35, 0
	v_mov_b32_e32 v36, 0
	v_mov_b32_e32 v37, 0
	v_mov_b32_e32 v42, 0
	v_mov_b32_e32 v43, 0
	v_mov_b32_e32 v44, 0
	v_mov_b32_e32 v45, 0
	s_mov_b32 s94, 86016
	s_mov_b32 s95, 0
	s_mov_b32 s91, 28672
	s_mov_b32 s25, 57344
	s_barrier
	s_cmp_gt_u32 s84, 3
	s_cbranch_scc1 .Lrt_path3
	s_add_i32 s39, s39, 0x80
	s_and_b32 s39, s39, 0x1fff
	s_add_u32 s40, s86, s39
	s_addc_u32 s41, s87, 0
	s_add_i32 m0, s94, s98
	s_nop 0
	global_load_lds_dwordx4 v208, s[40:41]
	s_add_i32 m0, s94, s99
	s_nop 0
	global_load_lds_dwordx4 v209, s[40:41]
	s_add_i32 m0, s94, s100
	s_nop 0
	global_load_lds_dwordx4 v210, s[40:41]
	s_add_i32 m0, s94, s101
	s_nop 0
	global_load_lds_dwordx4 v211, s[40:41]
	v_add_u32_e32 v214, s95, v212
	v_add_u32_e32 v215, s95, v213
	ds_read_b128 v[38:41], v215
	ds_read_b128 v[58:61], v214 offset:0
	ds_read_b128 v[62:65], v214 offset:2048
	ds_read_b128 v[66:69], v214 offset:4096
	ds_read_b128 v[70:73], v214 offset:6144
	ds_read_b128 v[74:77], v214 offset:8192
	ds_read_b128 v[100:103], v214 offset:10240
	ds_read_b128 v[104:107], v214 offset:12288
	ds_read_b128 v[108:111], v214 offset:14336
	ds_read_b128 v[112:115], v214 offset:16384
	ds_read_b128 v[116:119], v214 offset:18432
	s_waitcnt vmcnt(8)
	s_waitcnt lgkmcnt(0)
	s_barrier
	s_mov_b32 s33, s94
	s_mov_b32 s94, s95
	s_mov_b32 s95, s91
	s_mov_b32 s91, s25
	s_mov_b32 s25, s33
	s_add_i32 s39, s39, 0x80
	s_and_b32 s39, s39, 0x1fff
	s_add_u32 s40, s86, s39
	s_addc_u32 s41, s87, 0
	s_add_i32 m0, s94, s98
	s_nop 0
	global_load_lds_dwordx4 v208, s[40:41]
	s_add_i32 m0, s94, s99
	s_nop 0
	global_load_lds_dwordx4 v209, s[40:41]
	s_add_i32 m0, s94, s100
	s_nop 0
	global_load_lds_dwordx4 v210, s[40:41]
	s_add_i32 m0, s94, s101
	s_nop 0
	global_load_lds_dwordx4 v211, s[40:41]
	v_add_u32_e32 v214, s95, v212
	v_add_u32_e32 v215, s95, v213
	ds_read_b128 v[226:229], v215
	ds_read_b128 v[230:233], v214 offset:0
	ds_read_b128 v[234:237], v214 offset:2048
	ds_read_b128 v[238:241], v214 offset:4096
	ds_read_b128 v[242:245], v214 offset:6144
	ds_read_b128 v[246:249], v214 offset:8192
	ds_read_b128 v[120:123], v214 offset:10240
	ds_read_b128 v[124:127], v214 offset:12288
	ds_read_b128 v[132:135], v214 offset:14336
	ds_read_b128 v[136:139], v214 offset:16384
	ds_read_b128 v[140:143], v214 offset:18432
	v_mfma_f32_16x16x32_bf16 v[18:21], v[38:41], v[58:61], v[18:21]
	v_mfma_f32_16x16x32_bf16 v[22:25], v[38:41], v[62:65], v[22:25]
	v_mfma_f32_16x16x32_bf16 v[26:29], v[38:41], v[66:69], v[26:29]
	v_mfma_f32_16x16x32_bf16 v[30:33], v[38:41], v[70:73], v[30:33]
	v_mfma_f32_16x16x32_bf16 v[34:37], v[38:41], v[74:77], v[34:37]
	v_mfma_f32_16x16x32_bf16 v[42:45], v[38:41], v[38:41], v[42:45]
	v_mfma_f32_16x16x32_bf16 v[18:21], v[38:41], v[100:103], v[18:21]
	v_mfma_f32_16x16x32_bf16 v[22:25], v[38:41], v[104:107], v[22:25]
	v_mfma_f32_16x16x32_bf16 v[26:29], v[38:41], v[108:111], v[26:29]
	v_mfma_f32_16x16x32_bf16 v[30:33], v[38:41], v[112:115], v[30:33]
	v_mfma_f32_16x16x32_bf16 v[34:37], v[38:41], v[116:119], v[34:37]
	s_waitcnt vmcnt(8)
	s_waitcnt lgkmcnt(0)
	s_barrier
	s_mov_b32 s33, s94
	s_mov_b32 s94, s95
	s_mov_b32 s95, s91
	s_mov_b32 s91, s25
	s_mov_b32 s25, s33
	s_add_i32 s39, s39, 0x80
	s_and_b32 s39, s39, 0x1fff
	s_add_u32 s40, s86, s39
	s_addc_u32 s41, s87, 0
	s_add_i32 m0, s94, s98
	s_nop 0
	global_load_lds_dwordx4 v208, s[40:41]
	s_add_i32 m0, s94, s99
	s_nop 0
	global_load_lds_dwordx4 v209, s[40:41]
	s_add_i32 m0, s94, s100
	s_nop 0
	global_load_lds_dwordx4 v210, s[40:41]
	s_add_i32 m0, s94, s101
	s_nop 0
	global_load_lds_dwordx4 v211, s[40:41]
	v_add_u32_e32 v214, s95, v212
	v_add_u32_e32 v215, s95, v213
	ds_read_b128 v[38:41], v215
	ds_read_b128 v[58:61], v214 offset:0
	ds_read_b128 v[62:65], v214 offset:2048
	ds_read_b128 v[66:69], v214 offset:4096
	ds_read_b128 v[70:73], v214 offset:6144
	ds_read_b128 v[74:77], v214 offset:8192
	ds_read_b128 v[100:103], v214 offset:10240
	ds_read_b128 v[104:107], v214 offset:12288
	ds_read_b128 v[108:111], v214 offset:14336
	ds_read_b128 v[112:115], v214 offset:16384
	ds_read_b128 v[116:119], v214 offset:18432
	v_mfma_f32_16x16x32_bf16 v[18:21], v[226:229], v[230:233], v[18:21]
	v_mfma_f32_16x16x32_bf16 v[22:25], v[226:229], v[234:237], v[22:25]
	v_mfma_f32_16x16x32_bf16 v[26:29], v[226:229], v[238:241], v[26:29]
	v_mfma_f32_16x16x32_bf16 v[30:33], v[226:229], v[242:245], v[30:33]
	v_mfma_f32_16x16x32_bf16 v[34:37], v[226:229], v[246:249], v[34:37]
	v_mfma_f32_16x16x32_bf16 v[42:45], v[226:229], v[226:229], v[42:45]
	v_mfma_f32_16x16x32_bf16 v[18:21], v[226:229], v[120:123], v[18:21]
	v_mfma_f32_16x16x32_bf16 v[22:25], v[226:229], v[124:127], v[22:25]
	v_mfma_f32_16x16x32_bf16 v[26:29], v[226:229], v[132:135], v[26:29]
	v_mfma_f32_16x16x32_bf16 v[30:33], v[226:229], v[136:139], v[30:33]
	v_mfma_f32_16x16x32_bf16 v[34:37], v[226:229], v[140:143], v[34:37]
	s_waitcnt vmcnt(8)
	s_waitcnt lgkmcnt(0)
	s_barrier
; __device__ __forceinline__ void rt_step(const RtLoad& L, const bf16_t* bh, const bf16_t* bl, f32x4 (&acc)[2][5], float (&ss)[2], int ko) {
;     RtW W;
; #pragma unroll
;     for (int n = 0; n < 5; ++n) { W.wh[n] = *(const bf16x8*)(bh + (size_t)n * 16 * D + ko); W.wl[n] = *(const bf16x8*)(bl + (size_t)n * 16 * D + ko); }
;     bf16x8 ahi[2], alo[2];
; #pragma unroll
;     for (int mi = 0; mi < 2; ++mi) { const u32x4 xw = L.x[mi]; const f32x4 xa = (f32x4){bflo(xw.x), bfhi(xw.x), bflo(xw.y), bfhi(xw.y)}, xb = (f32x4){bflo(xw.z), bfhi(xw.z), bflo(xw.w), bfhi(xw.w)};
;         ss[mi] += (xa.x * xa.x + xa.y * xa.y) + (xa.z * xa.z + xa.w * xa.w) + (xb.x * xb.x + xb.y * xb.y) + (xb.z * xb.z + xb.w * xb.w);
;         const float u[8] = {xa.x * L.g[0].x, xa.y * L.g[0].y, xa.z * L.g[0].z, xa.w * L.g[0].w, xb.x * L.g[1].x, xb.y * L.g[1].y, xb.z * L.g[1].z, xb.w * L.g[1].w};
;         unsigned hb[8]; float lo[8];
; #pragma unroll
;         for (int j = 0; j < 8; ++j) { hb[j] = f2bf(u[j]); lo[j] = u[j] - __builtin_bit_cast(float, hb[j] << 16); }
;         const u32x4 hw = (u32x4){hb[0] | (hb[1] << 16), hb[2] | (hb[3] << 16), hb[4] | (hb[5] << 16), hb[6] | (hb[7] << 16)};
;         const u32x4 lw = (u32x4){pk2(lo[0], lo[1]), pk2(lo[2], lo[3]), pk2(lo[4], lo[5]), pk2(lo[6], lo[7])};
; __device__ __forceinline__ void p5_router(Frame& F) {
;     ...
;         { const int tg = wave & 1, kq = wave >> 1, fr = lane & 15, fq = lane >> 4;
;           f32x4 acc[2][5];
; #pragma unroll
;           for (int a = 0; a < 2; ++a)
; #pragma unroll
;               for (int n = 0; n < 5; ++n) acc[a][n] = (f32x4){0.f, 0.f, 0.f, 0.f};
;           float ss[2] = {0.f, 0.f};
;           const size_t roff = (size_t)(m0 + 32 * tg + fr) * D + kq * 1024 + 8 * fq;
;           const bf16_t* h0 = H + roff; const bf16_t* h1 = h0 + (size_t)16 * D;
;           const float* gp = F.g_ffn + kq * 1024 + 8 * fq;
;           const bf16_t* bh = RBH + (size_t)fr * D + kq * 1024 + 8 * fq; const bf16_t* bl = RBL + (size_t)fr * D + kq * 1024 + 8 * fq;
;           RtLoad La, Lb; rt_load(La, h0, h1, gp, 0);
; #pragma unroll 1
;           for (int ks = 0; ks < 32; ks += 2) {
;               rt_load(Lb, h0, h1, gp, (ks + 1) * 32); rt_step(La, bh, bl, acc, ss, ks * 32);
;               if (ks + 2 < 32) rt_load(La, h0, h1, gp, (ks + 2) * 32);
;               rt_step(Lb, bh, bl, acc, ss, (ks + 1) * 32); }
	s_mov_b32 s33, s94
	s_mov_b32 s94, s95
	s_mov_b32 s95, s91
	s_mov_b32 s91, s25
	s_mov_b32 s25, s33
	s_add_i32 s39, s39, 0x80
	s_and_b32 s39, s39, 0x1fff
	s_add_u32 s40, s86, s39
	s_addc_u32 s41, s87, 0
	s_add_i32 m0, s94, s98
	s_nop 0
	global_load_lds_dwordx4 v208, s[40:41]
	s_add_i32 m0, s94, s99
	s_nop 0
	global_load_lds_dwordx4 v209, s[40:41]
	s_add_i32 m0, s94, s100
	s_nop 0
	global_load_lds_dwordx4 v210, s[40:41]
	s_add_i32 m0, s94, s101
	s_nop 0
	global_load_lds_dwordx4 v211, s[40:41]
	v_add_u32_e32 v214, s95, v212
	v_add_u32_e32 v215, s95, v213
	ds_read_b128 v[226:229], v215
	ds_read_b128 v[230:233], v214 offset:0
	ds_read_b128 v[234:237], v214 offset:2048
	ds_read_b128 v[238:241], v214 offset:4096
	ds_read_b128 v[242:245], v214 offset:6144
	ds_read_b128 v[246:249], v214 offset:8192
	ds_read_b128 v[120:123], v214 offset:10240
	ds_read_b128 v[124:127], v214 offset:12288
	ds_read_b128 v[132:135], v214 offset:14336
	ds_read_b128 v[136:139], v214 offset:16384
	ds_read_b128 v[140:143], v214 offset:18432
	v_mfma_f32_16x16x32_bf16 v[18:21], v[38:41], v[58:61], v[18:21]
	v_mfma_f32_16x16x32_bf16 v[22:25], v[38:41], v[62:65], v[22:25]
	v_mfma_f32_16x16x32_bf16 v[26:29], v[38:41], v[66:69], v[26:29]
	v_mfma_f32_16x16x32_bf16 v[30:33], v[38:41], v[70:73], v[30:33]
	v_mfma_f32_16x16x32_bf16 v[34:37], v[38:41], v[74:77], v[34:37]
	v_mfma_f32_16x16x32_bf16 v[42:45], v[38:41], v[38:41], v[42:45]
	v_mfma_f32_16x16x32_bf16 v[18:21], v[38:41], v[100:103], v[18:21]
	v_mfma_f32_16x16x32_bf16 v[22:25], v[38:41], v[104:107], v[22:25]
	v_mfma_f32_16x16x32_bf16 v[26:29], v[38:41], v[108:111], v[26:29]
	v_mfma_f32_16x16x32_bf16 v[30:33], v[38:41], v[112:115], v[30:33]
	v_mfma_f32_16x16x32_bf16 v[34:37], v[38:41], v[116:119], v[34:37]
	s_waitcnt vmcnt(8)
	s_waitcnt lgkmcnt(0)
	s_barrier
	s_mov_b32 s33, s94
	s_mov_b32 s94, s95
	s_mov_b32 s95, s91
	s_mov_b32 s91, s25
	s_mov_b32 s25, s33
	s_add_i32 s39, s39, 0x80
	s_and_b32 s39, s39, 0x1fff
	s_add_u32 s40, s86, s39
	s_addc_u32 s41, s87, 0
	s_add_i32 m0, s94, s98
	s_nop 0
	global_load_lds_dwordx4 v208, s[40:41]
	s_add_i32 m0, s94, s99
	s_nop 0
	global_load_lds_dwordx4 v209, s[40:41]
	s_add_i32 m0, s94, s100
	s_nop 0
	global_load_lds_dwordx4 v210, s[40:41]
	s_add_i32 m0, s94, s101
	s_nop 0
	global_load_lds_dwordx4 v211, s[40:41]
	v_add_u32_e32 v214, s95, v212
	v_add_u32_e32 v215, s95, v213
	ds_read_b128 v[38:41], v215
	ds_read_b128 v[58:61], v214 offset:0
	ds_read_b128 v[62:65], v214 offset:2048
	ds_read_b128 v[66:69], v214 offset:4096
	ds_read_b128 v[70:73], v214 offset:6144
	ds_read_b128 v[74:77], v214 offset:8192
	ds_read_b128 v[100:103], v214 offset:10240
	ds_read_b128 v[104:107], v214 offset:12288
	ds_read_b128 v[108:111], v214 offset:14336
	ds_read_b128 v[112:115], v214 offset:16384
	ds_read_b128 v[116:119], v214 offset:18432
	v_mfma_f32_16x16x32_bf16 v[18:21], v[226:229], v[230:233], v[18:21]
	v_mfma_f32_16x16x32_bf16 v[22:25], v[226:229], v[234:237], v[22:25]
	v_mfma_f32_16x16x32_bf16 v[26:29], v[226:229], v[238:241], v[26:29]
	v_mfma_f32_16x16x32_bf16 v[30:33], v[226:229], v[242:245], v[30:33]
	v_mfma_f32_16x16x32_bf16 v[34:37], v[226:229], v[246:249], v[34:37]
	v_mfma_f32_16x16x32_bf16 v[42:45], v[226:229], v[226:229], v[42:45]
	v_mfma_f32_16x16x32_bf16 v[18:21], v[226:229], v[120:123], v[18:21]
	v_mfma_f32_16x16x32_bf16 v[22:25], v[226:229], v[124:127], v[22:25]
	v_mfma_f32_16x16x32_bf16 v[26:29], v[226:229], v[132:135], v[26:29]
	v_mfma_f32_16x16x32_bf16 v[30:33], v[226:229], v[136:139], v[30:33]
	v_mfma_f32_16x16x32_bf16 v[34:37], v[226:229], v[140:143], v[34:37]
	s_waitcnt vmcnt(8)
	s_waitcnt lgkmcnt(0)
	s_barrier
	s_mov_b32 s33, s94
	s_mov_b32 s94, s95
	s_mov_b32 s95, s91
	s_mov_b32 s91, s25
	s_mov_b32 s25, s33
	s_mov_b32 s85, 13
.Lrt_loop_p4:
	s_add_i32 s39, s39, 0x80
	s_and_b32 s39, s39, 0x1fff
	s_add_u32 s40, s86, s39
	s_addc_u32 s41, s87, 0
	s_add_i32 m0, s94, s98
	s_nop 0
	global_load_lds_dwordx4 v208, s[40:41]
	s_add_i32 m0, s94, s99
	s_nop 0
	global_load_lds_dwordx4 v209, s[40:41]
	s_add_i32 m0, s94, s100
	s_nop 0
	global_load_lds_dwordx4 v210, s[40:41]
	s_add_i32 m0, s94, s101
	s_nop 0
	global_load_lds_dwordx4 v211, s[40:41]
	v_add_u32_e32 v214, s95, v212
	v_add_u32_e32 v215, s95, v213
	ds_read_b128 v[226:229], v215
	ds_read_b128 v[230:233], v214 offset:0
	ds_read_b128 v[234:237], v214 offset:2048
	ds_read_b128 v[238:241], v214 offset:4096
	ds_read_b128 v[242:245], v214 offset:6144
	ds_read_b128 v[246:249], v214 offset:8192
	ds_read_b128 v[120:123], v214 offset:10240
	ds_read_b128 v[124:127], v214 offset:12288
	ds_read_b128 v[132:135], v214 offset:14336
	ds_read_b128 v[136:139], v214 offset:16384
	ds_read_b128 v[140:143], v214 offset:18432
	v_mfma_f32_16x16x32_bf16 v[18:21], v[38:41], v[58:61], v[18:21]
	v_mfma_f32_16x16x32_bf16 v[22:25], v[38:41], v[62:65], v[22:25]
	v_mfma_f32_16x16x32_bf16 v[26:29], v[38:41], v[66:69], v[26:29]
	v_mfma_f32_16x16x32_bf16 v[30:33], v[38:41], v[70:73], v[30:33]
	v_mfma_f32_16x16x32_bf16 v[34:37], v[38:41], v[74:77], v[34:37]
	v_mfma_f32_16x16x32_bf16 v[42:45], v[38:41], v[38:41], v[42:45]
	v_mfma_f32_16x16x32_bf16 v[18:21], v[38:41], v[100:103], v[18:21]
	v_mfma_f32_16x16x32_bf16 v[22:25], v[38:41], v[104:107], v[22:25]
	v_mfma_f32_16x16x32_bf16 v[26:29], v[38:41], v[108:111], v[26:29]
	v_mfma_f32_16x16x32_bf16 v[30:33], v[38:41], v[112:115], v[30:33]
	v_mfma_f32_16x16x32_bf16 v[34:37], v[38:41], v[116:119], v[34:37]
	s_waitcnt vmcnt(8)
	s_waitcnt lgkmcnt(0)
	s_barrier
; __device__ __forceinline__ void rt_step(const RtLoad& L, const bf16_t* bh, const bf16_t* bl, f32x4 (&acc)[2][5], float (&ss)[2], int ko) {
;     RtW W;
; #pragma unroll
;     for (int n = 0; n < 5; ++n) { W.wh[n] = *(const bf16x8*)(bh + (size_t)n * 16 * D + ko); W.wl[n] = *(const bf16x8*)(bl + (size_t)n * 16 * D + ko); }
;     bf16x8 ahi[2], alo[2];
; #pragma unroll
;     for (int mi = 0; mi < 2; ++mi) { const u32x4 xw = L.x[mi]; const f32x4 xa = (f32x4){bflo(xw.x), bfhi(xw.x), bflo(xw.y), bfhi(xw.y)}, xb = (f32x4){bflo(xw.z), bfhi(xw.z), bflo(xw.w), bfhi(xw.w)};
;         ss[mi] += (xa.x * xa.x + xa.y * xa.y) + (xa.z * xa.z + xa.w * xa.w) + (xb.x * xb.x + xb.y * xb.y) + (xb.z * xb.z + xb.w * xb.w);
;         const float u[8] = {xa.x * L.g[0].x, xa.y * L.g[0].y, xa.z * L.g[0].z, xa.w * L.g[0].w, xb.x * L.g[1].x, xb.y * L.g[1].y, xb.z * L.g[1].z, xb.w * L.g[1].w};
;         unsigned hb[8]; float lo[8];
; #pragma unroll
;         for (int j = 0; j < 8; ++j) { hb[j] = f2bf(u[j]); lo[j] = u[j] - __builtin_bit_cast(float, hb[j] << 16); }
;         const u32x4 hw = (u32x4){hb[0] | (hb[1] << 16), hb[2] | (hb[3] << 16), hb[4] | (hb[5] << 16), hb[6] | (hb[7] << 16)};
;         const u32x4 lw = (u32x4){pk2(lo[0], lo[1]), pk2(lo[2], lo[3]), pk2(lo[4], lo[5]), pk2(lo[6], lo[7])};
; __device__ __forceinline__ void p5_router(Frame& F) {
;     ...
;         { const int tg = wave & 1, kq = wave >> 1, fr = lane & 15, fq = lane >> 4;
;           f32x4 acc[2][5];
; #pragma unroll
;           for (int a = 0; a < 2; ++a)
; #pragma unroll
;               for (int n = 0; n < 5; ++n) acc[a][n] = (f32x4){0.f, 0.f, 0.f, 0.f};
;           float ss[2] = {0.f, 0.f};
;           const size_t roff = (size_t)(m0 + 32 * tg + fr) * D + kq * 1024 + 8 * fq;
;           const bf16_t* h0 = H + roff; const bf16_t* h1 = h0 + (size_t)16 * D;
;           const float* gp = F.g_ffn + kq * 1024 + 8 * fq;
;           const bf16_t* bh = RBH + (size_t)fr * D + kq * 1024 + 8 * fq; const bf16_t* bl = RBL + (size_t)fr * D + kq * 1024 + 8 * fq;
;           RtLoad La, Lb; rt_load(La, h0, h1, gp, 0);
; #pragma unroll 1
;           for (int ks = 0; ks < 32; ks += 2) {
;               rt_load(Lb, h0, h1, gp, (ks + 1) * 32); rt_step(La, bh, bl, acc, ss, ks * 32);
;               if (ks + 2 < 32) rt_load(La, h0, h1, gp, (ks + 2) * 32);
;               rt_step(Lb, bh, bl, acc, ss, (ks + 1) * 32); }
	s_mov_b32 s33, s94
	s_mov_b32 s94, s95
	s_mov_b32 s95, s91
	s_mov_b32 s91, s25
	s_mov_b32 s25, s33
	s_add_i32 s39, s39, 0x80
	s_and_b32 s39, s39, 0x1fff
	s_add_u32 s40, s86, s39
	s_addc_u32 s41, s87, 0
	s_add_i32 m0, s94, s98
	s_nop 0
	global_load_lds_dwordx4 v208, s[40:41]
	s_add_i32 m0, s94, s99
	s_nop 0
	global_load_lds_dwordx4 v209, s[40:41]
	s_add_i32 m0, s94, s100
	s_nop 0
	global_load_lds_dwordx4 v210, s[40:41]
	s_add_i32 m0, s94, s101
	s_nop 0
	global_load_lds_dwordx4 v211, s[40:41]
	v_add_u32_e32 v214, s95, v212
	v_add_u32_e32 v215, s95, v213
	ds_read_b128 v[38:41], v215
	ds_read_b128 v[58:61], v214 offset:0
	ds_read_b128 v[62:65], v214 offset:2048
	ds_read_b128 v[66:69], v214 offset:4096
	ds_read_b128 v[70:73], v214 offset:6144
	ds_read_b128 v[74:77], v214 offset:8192
	ds_read_b128 v[100:103], v214 offset:10240
	ds_read_b128 v[104:107], v214 offset:12288
	ds_read_b128 v[108:111], v214 offset:14336
	ds_read_b128 v[112:115], v214 offset:16384
	ds_read_b128 v[116:119], v214 offset:18432
	v_mfma_f32_16x16x32_bf16 v[18:21], v[226:229], v[230:233], v[18:21]
	v_mfma_f32_16x16x32_bf16 v[22:25], v[226:229], v[234:237], v[22:25]
	v_mfma_f32_16x16x32_bf16 v[26:29], v[226:229], v[238:241], v[26:29]
	v_mfma_f32_16x16x32_bf16 v[30:33], v[226:229], v[242:245], v[30:33]
	v_mfma_f32_16x16x32_bf16 v[34:37], v[226:229], v[246:249], v[34:37]
	v_mfma_f32_16x16x32_bf16 v[42:45], v[226:229], v[226:229], v[42:45]
	v_mfma_f32_16x16x32_bf16 v[18:21], v[226:229], v[120:123], v[18:21]
	v_mfma_f32_16x16x32_bf16 v[22:25], v[226:229], v[124:127], v[22:25]
	v_mfma_f32_16x16x32_bf16 v[26:29], v[226:229], v[132:135], v[26:29]
	v_mfma_f32_16x16x32_bf16 v[30:33], v[226:229], v[136:139], v[30:33]
	v_mfma_f32_16x16x32_bf16 v[34:37], v[226:229], v[140:143], v[34:37]
	s_waitcnt vmcnt(8)
	s_waitcnt lgkmcnt(0)
	s_barrier
	s_mov_b32 s33, s94
	s_mov_b32 s94, s95
	s_mov_b32 s95, s91
	s_mov_b32 s91, s25
	s_mov_b32 s25, s33
	s_add_i32 s39, s39, 0x80
	s_and_b32 s39, s39, 0x1fff
	s_add_u32 s40, s86, s39
	s_addc_u32 s41, s87, 0
	s_add_i32 m0, s94, s98
	s_nop 0
	global_load_lds_dwordx4 v208, s[40:41]
	s_add_i32 m0, s94, s99
	s_nop 0
	global_load_lds_dwordx4 v209, s[40:41]
	s_add_i32 m0, s94, s100
	s_nop 0
	global_load_lds_dwordx4 v210, s[40:41]
	s_add_i32 m0, s94, s101
	s_nop 0
	global_load_lds_dwordx4 v211, s[40:41]
	v_add_u32_e32 v214, s95, v212
	v_add_u32_e32 v215, s95, v213
	ds_read_b128 v[226:229], v215
	ds_read_b128 v[230:233], v214 offset:0
	ds_read_b128 v[234:237], v214 offset:2048
	ds_read_b128 v[238:241], v214 offset:4096
	ds_read_b128 v[242:245], v214 offset:6144
	ds_read_b128 v[246:249], v214 offset:8192
	ds_read_b128 v[120:123], v214 offset:10240
	ds_read_b128 v[124:127], v214 offset:12288
	ds_read_b128 v[132:135], v214 offset:14336
	ds_read_b128 v[136:139], v214 offset:16384
	ds_read_b128 v[140:143], v214 offset:18432
	v_mfma_f32_16x16x32_bf16 v[18:21], v[38:41], v[58:61], v[18:21]
	v_mfma_f32_16x16x32_bf16 v[22:25], v[38:41], v[62:65], v[22:25]
	v_mfma_f32_16x16x32_bf16 v[26:29], v[38:41], v[66:69], v[26:29]
	v_mfma_f32_16x16x32_bf16 v[30:33], v[38:41], v[70:73], v[30:33]
	v_mfma_f32_16x16x32_bf16 v[34:37], v[38:41], v[74:77], v[34:37]
	v_mfma_f32_16x16x32_bf16 v[42:45], v[38:41], v[38:41], v[42:45]
	v_mfma_f32_16x16x32_bf16 v[18:21], v[38:41], v[100:103], v[18:21]
	v_mfma_f32_16x16x32_bf16 v[22:25], v[38:41], v[104:107], v[22:25]
	v_mfma_f32_16x16x32_bf16 v[26:29], v[38:41], v[108:111], v[26:29]
	v_mfma_f32_16x16x32_bf16 v[30:33], v[38:41], v[112:115], v[30:33]
	v_mfma_f32_16x16x32_bf16 v[34:37], v[38:41], v[116:119], v[34:37]
	s_waitcnt vmcnt(8)
	s_waitcnt lgkmcnt(0)
	s_barrier
	s_mov_b32 s33, s94
	s_mov_b32 s94, s95
	s_mov_b32 s95, s91
	s_mov_b32 s91, s25
	s_mov_b32 s25, s33
	s_add_i32 s39, s39, 0x80
	s_and_b32 s39, s39, 0x1fff
	s_add_u32 s40, s86, s39
	s_addc_u32 s41, s87, 0
	s_add_i32 m0, s94, s98
	s_nop 0
	global_load_lds_dwordx4 v208, s[40:41]
	s_add_i32 m0, s94, s99
	s_nop 0
	global_load_lds_dwordx4 v209, s[40:41]
	s_add_i32 m0, s94, s100
	s_nop 0
	global_load_lds_dwordx4 v210, s[40:41]
	s_add_i32 m0, s94, s101
	s_nop 0
	global_load_lds_dwordx4 v211, s[40:41]
	v_add_u32_e32 v214, s95, v212
	v_add_u32_e32 v215, s95, v213
	ds_read_b128 v[38:41], v215
	ds_read_b128 v[58:61], v214 offset:0
	ds_read_b128 v[62:65], v214 offset:2048
	ds_read_b128 v[66:69], v214 offset:4096
	ds_read_b128 v[70:73], v214 offset:6144
	ds_read_b128 v[74:77], v214 offset:8192
	ds_read_b128 v[100:103], v214 offset:10240
	ds_read_b128 v[104:107], v214 offset:12288
	ds_read_b128 v[108:111], v214 offset:14336
	ds_read_b128 v[112:115], v214 offset:16384
	ds_read_b128 v[116:119], v214 offset:18432
	v_mfma_f32_16x16x32_bf16 v[18:21], v[226:229], v[230:233], v[18:21]
	v_mfma_f32_16x16x32_bf16 v[22:25], v[226:229], v[234:237], v[22:25]
	v_mfma_f32_16x16x32_bf16 v[26:29], v[226:229], v[238:241], v[26:29]
	v_mfma_f32_16x16x32_bf16 v[30:33], v[226:229], v[242:245], v[30:33]
	v_mfma_f32_16x16x32_bf16 v[34:37], v[226:229], v[246:249], v[34:37]
	v_mfma_f32_16x16x32_bf16 v[42:45], v[226:229], v[226:229], v[42:45]
	v_mfma_f32_16x16x32_bf16 v[18:21], v[226:229], v[120:123], v[18:21]
	v_mfma_f32_16x16x32_bf16 v[22:25], v[226:229], v[124:127], v[22:25]
	v_mfma_f32_16x16x32_bf16 v[26:29], v[226:229], v[132:135], v[26:29]
	v_mfma_f32_16x16x32_bf16 v[30:33], v[226:229], v[136:139], v[30:33]
	v_mfma_f32_16x16x32_bf16 v[34:37], v[226:229], v[140:143], v[34:37]
	s_waitcnt vmcnt(8)
	s_waitcnt lgkmcnt(0)
	s_barrier
	s_mov_b32 s33, s94
	s_mov_b32 s94, s95
	s_mov_b32 s95, s91
	s_mov_b32 s91, s25
	s_mov_b32 s25, s33
	s_sub_u32 s85, s85, 1
	s_cmp_lg_u32 s85, 0
	s_cbranch_scc1 .Lrt_loop_p4
; __device__ __forceinline__ void rt_step(const RtLoad& L, const bf16_t* bh, const bf16_t* bl, f32x4 (&acc)[2][5], float (&ss)[2], int ko) {
;     RtW W;
; #pragma unroll
;     for (int n = 0; n < 5; ++n) { W.wh[n] = *(const bf16x8*)(bh + (size_t)n * 16 * D + ko); W.wl[n] = *(const bf16x8*)(bl + (size_t)n * 16 * D + ko); }
;     bf16x8 ahi[2], alo[2];
; #pragma unroll
;     for (int mi = 0; mi < 2; ++mi) { const u32x4 xw = L.x[mi]; const f32x4 xa = (f32x4){bflo(xw.x), bfhi(xw.x), bflo(xw.y), bfhi(xw.y)}, xb = (f32x4){bflo(xw.z), bfhi(xw.z), bflo(xw.w), bfhi(xw.w)};
;         ss[mi] += (xa.x * xa.x + xa.y * xa.y) + (xa.z * xa.z + xa.w * xa.w) + (xb.x * xb.x + xb.y * xb.y) + (xb.z * xb.z + xb.w * xb.w);
;         const float u[8] = {xa.x * L.g[0].x, xa.y * L.g[0].y, xa.z * L.g[0].z, xa.w * L.g[0].w, xb.x * L.g[1].x, xb.y * L.g[1].y, xb.z * L.g[1].z, xb.w * L.g[1].w};
;         unsigned hb[8]; float lo[8];
; #pragma unroll
;         for (int j = 0; j < 8; ++j) { hb[j] = f2bf(u[j]); lo[j] = u[j] - __builtin_bit_cast(float, hb[j] << 16); }
;         const u32x4 hw = (u32x4){hb[0] | (hb[1] << 16), hb[2] | (hb[3] << 16), hb[4] | (hb[5] << 16), hb[6] | (hb[7] << 16)};
;         const u32x4 lw = (u32x4){pk2(lo[0], lo[1]), pk2(lo[2], lo[3]), pk2(lo[4], lo[5]), pk2(lo[6], lo[7])};
; __device__ __forceinline__ void p5_router(Frame& F) {
;     ...
;         { const int tg = wave & 1, kq = wave >> 1, fr = lane & 15, fq = lane >> 4;
;           f32x4 acc[2][5];
; #pragma unroll
;           for (int a = 0; a < 2; ++a)
; #pragma unroll
;               for (int n = 0; n < 5; ++n) acc[a][n] = (f32x4){0.f, 0.f, 0.f, 0.f};
;           float ss[2] = {0.f, 0.f};
;           const size_t roff = (size_t)(m0 + 32 * tg + fr) * D + kq * 1024 + 8 * fq;
;           const bf16_t* h0 = H + roff; const bf16_t* h1 = h0 + (size_t)16 * D;
;           const float* gp = F.g_ffn + kq * 1024 + 8 * fq;
;           const bf16_t* bh = RBH + (size_t)fr * D + kq * 1024 + 8 * fq; const bf16_t* bl = RBL + (size_t)fr * D + kq * 1024 + 8 * fq;
;           RtLoad La, Lb; rt_load(La, h0, h1, gp, 0);
; #pragma unroll 1
;           for (int ks = 0; ks < 32; ks += 2) {
;               rt_load(Lb, h0, h1, gp, (ks + 1) * 32); rt_step(La, bh, bl, acc, ss, ks * 32);
;               if (ks + 2 < 32) rt_load(La, h0, h1, gp, (ks + 2) * 32);
;               rt_step(Lb, bh, bl, acc, ss, (ks + 1) * 32); }
	s_add_i32 s39, s39, 0x80
	s_and_b32 s39, s39, 0x1fff
	s_add_u32 s40, s86, s39
	s_addc_u32 s41, s87, 0
	s_add_i32 m0, s94, s98
	s_nop 0
	global_load_lds_dwordx4 v208, s[40:41]
	s_add_i32 m0, s94, s99
	s_nop 0
	global_load_lds_dwordx4 v209, s[40:41]
	s_add_i32 m0, s94, s100
	s_nop 0
	global_load_lds_dwordx4 v210, s[40:41]
	s_add_i32 m0, s94, s101
	s_nop 0
	global_load_lds_dwordx4 v211, s[40:41]
	v_add_u32_e32 v214, s95, v212
	v_add_u32_e32 v215, s95, v213
	ds_read_b128 v[226:229], v215
	ds_read_b128 v[230:233], v214 offset:0
	ds_read_b128 v[234:237], v214 offset:2048
	ds_read_b128 v[238:241], v214 offset:4096
	ds_read_b128 v[242:245], v214 offset:6144
	ds_read_b128 v[246:249], v214 offset:8192
	ds_read_b128 v[120:123], v214 offset:10240
	ds_read_b128 v[124:127], v214 offset:12288
	ds_read_b128 v[132:135], v214 offset:14336
	ds_read_b128 v[136:139], v214 offset:16384
	ds_read_b128 v[140:143], v214 offset:18432
	v_mfma_f32_16x16x32_bf16 v[18:21], v[38:41], v[58:61], v[18:21]
	v_mfma_f32_16x16x32_bf16 v[22:25], v[38:41], v[62:65], v[22:25]
	v_mfma_f32_16x16x32_bf16 v[26:29], v[38:41], v[66:69], v[26:29]
	v_mfma_f32_16x16x32_bf16 v[30:33], v[38:41], v[70:73], v[30:33]
	v_mfma_f32_16x16x32_bf16 v[34:37], v[38:41], v[74:77], v[34:37]
	v_mfma_f32_16x16x32_bf16 v[42:45], v[38:41], v[38:41], v[42:45]
	v_mfma_f32_16x16x32_bf16 v[18:21], v[38:41], v[100:103], v[18:21]
	v_mfma_f32_16x16x32_bf16 v[22:25], v[38:41], v[104:107], v[22:25]
	v_mfma_f32_16x16x32_bf16 v[26:29], v[38:41], v[108:111], v[26:29]
	v_mfma_f32_16x16x32_bf16 v[30:33], v[38:41], v[112:115], v[30:33]
	v_mfma_f32_16x16x32_bf16 v[34:37], v[38:41], v[116:119], v[34:37]
	s_waitcnt vmcnt(8)
	s_waitcnt lgkmcnt(0)
	s_barrier
	s_mov_b32 s33, s94
	s_mov_b32 s94, s95
	s_mov_b32 s95, s91
	s_mov_b32 s91, s25
	s_mov_b32 s25, s33
	s_add_i32 s39, s39, 0x80
	s_and_b32 s39, s39, 0x1fff
	s_add_u32 s40, s86, s39
	s_addc_u32 s41, s87, 0
	s_add_i32 m0, s94, s98
	s_nop 0
	global_load_lds_dwordx4 v208, s[40:41]
	s_add_i32 m0, s94, s99
	s_nop 0
	global_load_lds_dwordx4 v209, s[40:41]
	s_add_i32 m0, s94, s100
	s_nop 0
	global_load_lds_dwordx4 v210, s[40:41]
	s_add_i32 m0, s94, s101
	s_nop 0
	global_load_lds_dwordx4 v211, s[40:41]
	v_add_u32_e32 v214, s95, v212
	v_add_u32_e32 v215, s95, v213
	ds_read_b128 v[38:41], v215
	ds_read_b128 v[58:61], v214 offset:0
	ds_read_b128 v[62:65], v214 offset:2048
	ds_read_b128 v[66:69], v214 offset:4096
	ds_read_b128 v[70:73], v214 offset:6144
	ds_read_b128 v[74:77], v214 offset:8192
	ds_read_b128 v[100:103], v214 offset:10240
	ds_read_b128 v[104:107], v214 offset:12288
	ds_read_b128 v[108:111], v214 offset:14336
	ds_read_b128 v[112:115], v214 offset:16384
	ds_read_b128 v[116:119], v214 offset:18432
	v_mfma_f32_16x16x32_bf16 v[18:21], v[226:229], v[230:233], v[18:21]
	v_mfma_f32_16x16x32_bf16 v[22:25], v[226:229], v[234:237], v[22:25]
	v_mfma_f32_16x16x32_bf16 v[26:29], v[226:229], v[238:241], v[26:29]
	v_mfma_f32_16x16x32_bf16 v[30:33], v[226:229], v[242:245], v[30:33]
	v_mfma_f32_16x16x32_bf16 v[34:37], v[226:229], v[246:249], v[34:37]
	v_mfma_f32_16x16x32_bf16 v[42:45], v[226:229], v[226:229], v[42:45]
	v_mfma_f32_16x16x32_bf16 v[18:21], v[226:229], v[120:123], v[18:21]
	v_mfma_f32_16x16x32_bf16 v[22:25], v[226:229], v[124:127], v[22:25]
	v_mfma_f32_16x16x32_bf16 v[26:29], v[226:229], v[132:135], v[26:29]
	v_mfma_f32_16x16x32_bf16 v[30:33], v[226:229], v[136:139], v[30:33]
	v_mfma_f32_16x16x32_bf16 v[34:37], v[226:229], v[140:143], v[34:37]
	s_waitcnt vmcnt(8)
	s_waitcnt lgkmcnt(0)
	s_barrier
	s_mov_b32 s33, s94
	s_mov_b32 s94, s95
	s_mov_b32 s95, s91
	s_mov_b32 s91, s25
	s_mov_b32 s25, s33
	s_add_i32 s39, s39, 0x80
	s_and_b32 s39, s39, 0x1fff
	s_add_u32 s40, s86, s39
	s_addc_u32 s41, s87, 0
	s_add_i32 m0, s94, s98
	s_nop 0
	global_load_lds_dwordx4 v208, s[40:41]
	s_add_i32 m0, s94, s99
	s_nop 0
	global_load_lds_dwordx4 v209, s[40:41]
	s_add_i32 m0, s94, s100
	s_nop 0
	global_load_lds_dwordx4 v210, s[40:41]
	s_add_i32 m0, s94, s101
	s_nop 0
	global_load_lds_dwordx4 v211, s[40:41]
	v_add_u32_e32 v214, s95, v212
	v_add_u32_e32 v215, s95, v213
	ds_read_b128 v[226:229], v215
	ds_read_b128 v[230:233], v214 offset:0
	ds_read_b128 v[234:237], v214 offset:2048
	ds_read_b128 v[238:241], v214 offset:4096
	ds_read_b128 v[242:245], v214 offset:6144
	ds_read_b128 v[246:249], v214 offset:8192
	ds_read_b128 v[120:123], v214 offset:10240
	ds_read_b128 v[124:127], v214 offset:12288
	ds_read_b128 v[132:135], v214 offset:14336
	ds_read_b128 v[136:139], v214 offset:16384
	ds_read_b128 v[140:143], v214 offset:18432
	v_mfma_f32_16x16x32_bf16 v[18:21], v[38:41], v[58:61], v[18:21]
	v_mfma_f32_16x16x32_bf16 v[22:25], v[38:41], v[62:65], v[22:25]
	v_mfma_f32_16x16x32_bf16 v[26:29], v[38:41], v[66:69], v[26:29]
	v_mfma_f32_16x16x32_bf16 v[30:33], v[38:41], v[70:73], v[30:33]
	v_mfma_f32_16x16x32_bf16 v[34:37], v[38:41], v[74:77], v[34:37]
	v_mfma_f32_16x16x32_bf16 v[42:45], v[38:41], v[38:41], v[42:45]
	v_mfma_f32_16x16x32_bf16 v[18:21], v[38:41], v[100:103], v[18:21]
	v_mfma_f32_16x16x32_bf16 v[22:25], v[38:41], v[104:107], v[22:25]
	v_mfma_f32_16x16x32_bf16 v[26:29], v[38:41], v[108:111], v[26:29]
	v_mfma_f32_16x16x32_bf16 v[30:33], v[38:41], v[112:115], v[30:33]
	v_mfma_f32_16x16x32_bf16 v[34:37], v[38:41], v[116:119], v[34:37]
	s_waitcnt vmcnt(8)
	s_waitcnt lgkmcnt(0)
	s_barrier
; __device__ __forceinline__ void rt_step(const RtLoad& L, const bf16_t* bh, const bf16_t* bl, f32x4 (&acc)[2][5], float (&ss)[2], int ko) {
;     RtW W;
; #pragma unroll
;     for (int n = 0; n < 5; ++n) { W.wh[n] = *(const bf16x8*)(bh + (size_t)n * 16 * D + ko); W.wl[n] = *(const bf16x8*)(bl + (size_t)n * 16 * D + ko); }
;     bf16x8 ahi[2], alo[2];
; #pragma unroll
;     for (int mi = 0; mi < 2; ++mi) { const u32x4 xw = L.x[mi]; const f32x4 xa = (f32x4){bflo(xw.x), bfhi(xw.x), bflo(xw.y), bfhi(xw.y)}, xb = (f32x4){bflo(xw.z), bfhi(xw.z), bflo(xw.w), bfhi(xw.w)};
;         ss[mi] += (xa.x * xa.x + xa.y * xa.y) + (xa.z * xa.z + xa.w * xa.w) + (xb.x * xb.x + xb.y * xb.y) + (xb.z * xb.z + xb.w * xb.w);
;         const float u[8] = {xa.x * L.g[0].x, xa.y * L.g[0].y, xa.z * L.g[0].z, xa.w * L.g[0].w, xb.x * L.g[1].x, xb.y * L.g[1].y, xb.z * L.g[1].z, xb.w * L.g[1].w};
;         unsigned hb[8]; float lo[8];
; #pragma unroll
;         for (int j = 0; j < 8; ++j) { hb[j] = f2bf(u[j]); lo[j] = u[j] - __builtin_bit_cast(float, hb[j] << 16); }
;         const u32x4 hw = (u32x4){hb[0] | (hb[1] << 16), hb[2] | (hb[3] << 16), hb[4] | (hb[5] << 16), hb[6] | (hb[7] << 16)};
;         const u32x4 lw = (u32x4){pk2(lo[0], lo[1]), pk2(lo[2], lo[3]), pk2(lo[4], lo[5]), pk2(lo[6], lo[7])};
; __device__ __forceinline__ void p5_router(Frame& F) {
;     ...
;         { const int tg = wave & 1, kq = wave >> 1, fr = lane & 15, fq = lane >> 4;
;           f32x4 acc[2][5];
; #pragma unroll
;           for (int a = 0; a < 2; ++a)
; #pragma unroll
;               for (int n = 0; n < 5; ++n) acc[a][n] = (f32x4){0.f, 0.f, 0.f, 0.f};
;           float ss[2] = {0.f, 0.f};
;           const size_t roff = (size_t)(m0 + 32 * tg + fr) * D + kq * 1024 + 8 * fq;
;           const bf16_t* h0 = H + roff; const bf16_t* h1 = h0 + (size_t)16 * D;
;           const float* gp = F.g_ffn + kq * 1024 + 8 * fq;
;           const bf16_t* bh = RBH + (size_t)fr * D + kq * 1024 + 8 * fq; const bf16_t* bl = RBL + (size_t)fr * D + kq * 1024 + 8 * fq;
;           RtLoad La, Lb; rt_load(La, h0, h1, gp, 0);
; #pragma unroll 1
;           for (int ks = 0; ks < 32; ks += 2) {
;               rt_load(Lb, h0, h1, gp, (ks + 1) * 32); rt_step(La, bh, bl, acc, ss, ks * 32);
;               if (ks + 2 < 32) rt_load(La, h0, h1, gp, (ks + 2) * 32);
;               rt_step(Lb, bh, bl, acc, ss, (ks + 1) * 32); }
	s_mov_b32 s33, s94
	s_mov_b32 s94, s95
	s_mov_b32 s95, s91
	s_mov_b32 s91, s25
	s_mov_b32 s25, s33
	s_add_i32 s39, s39, 0x80
	s_and_b32 s39, s39, 0x1fff
	s_add_u32 s40, s86, s39
	s_addc_u32 s41, s87, 0
	s_add_i32 m0, s94, s98
	s_nop 0
	global_load_lds_dwordx4 v208, s[40:41]
	s_add_i32 m0, s94, s99
	s_nop 0
	global_load_lds_dwordx4 v209, s[40:41]
	s_add_i32 m0, s94, s100
	s_nop 0
	global_load_lds_dwordx4 v210, s[40:41]
	s_add_i32 m0, s94, s101
	s_nop 0
	global_load_lds_dwordx4 v211, s[40:41]
	v_add_u32_e32 v214, s95, v212
	v_add_u32_e32 v215, s95, v213
	ds_read_b128 v[38:41], v215
	ds_read_b128 v[58:61], v214 offset:0
	ds_read_b128 v[62:65], v214 offset:2048
	ds_read_b128 v[66:69], v214 offset:4096
	ds_read_b128 v[70:73], v214 offset:6144
	ds_read_b128 v[74:77], v214 offset:8192
	ds_read_b128 v[100:103], v214 offset:10240
	ds_read_b128 v[104:107], v214 offset:12288
	ds_read_b128 v[108:111], v214 offset:14336
	ds_read_b128 v[112:115], v214 offset:16384
	ds_read_b128 v[116:119], v214 offset:18432
	v_mfma_f32_16x16x32_bf16 v[18:21], v[226:229], v[230:233], v[18:21]
	v_mfma_f32_16x16x32_bf16 v[22:25], v[226:229], v[234:237], v[22:25]
	v_mfma_f32_16x16x32_bf16 v[26:29], v[226:229], v[238:241], v[26:29]
	v_mfma_f32_16x16x32_bf16 v[30:33], v[226:229], v[242:245], v[30:33]
	v_mfma_f32_16x16x32_bf16 v[34:37], v[226:229], v[246:249], v[34:37]
	v_mfma_f32_16x16x32_bf16 v[42:45], v[226:229], v[226:229], v[42:45]
	v_mfma_f32_16x16x32_bf16 v[18:21], v[226:229], v[120:123], v[18:21]
	v_mfma_f32_16x16x32_bf16 v[22:25], v[226:229], v[124:127], v[22:25]
	v_mfma_f32_16x16x32_bf16 v[26:29], v[226:229], v[132:135], v[26:29]
	v_mfma_f32_16x16x32_bf16 v[30:33], v[226:229], v[136:139], v[30:33]
	v_mfma_f32_16x16x32_bf16 v[34:37], v[226:229], v[140:143], v[34:37]
	s_waitcnt vmcnt(8)
	s_waitcnt lgkmcnt(0)
	s_barrier
	s_mov_b32 s33, s94
	s_mov_b32 s94, s95
	s_mov_b32 s95, s91
	s_mov_b32 s91, s25
	s_mov_b32 s25, s33
	v_add_u32_e32 v214, s95, v212
	v_add_u32_e32 v215, s95, v213
	ds_read_b128 v[226:229], v215
	ds_read_b128 v[230:233], v214 offset:0
	ds_read_b128 v[234:237], v214 offset:2048
	ds_read_b128 v[238:241], v214 offset:4096
	ds_read_b128 v[242:245], v214 offset:6144
	ds_read_b128 v[246:249], v214 offset:8192
	ds_read_b128 v[120:123], v214 offset:10240
	ds_read_b128 v[124:127], v214 offset:12288
	ds_read_b128 v[132:135], v214 offset:14336
	ds_read_b128 v[136:139], v214 offset:16384
	ds_read_b128 v[140:143], v214 offset:18432
	v_mfma_f32_16x16x32_bf16 v[18:21], v[38:41], v[58:61], v[18:21]
	v_mfma_f32_16x16x32_bf16 v[22:25], v[38:41], v[62:65], v[22:25]
	v_mfma_f32_16x16x32_bf16 v[26:29], v[38:41], v[66:69], v[26:29]
	v_mfma_f32_16x16x32_bf16 v[30:33], v[38:41], v[70:73], v[30:33]
	v_mfma_f32_16x16x32_bf16 v[34:37], v[38:41], v[74:77], v[34:37]
	v_mfma_f32_16x16x32_bf16 v[42:45], v[38:41], v[38:41], v[42:45]
	v_mfma_f32_16x16x32_bf16 v[18:21], v[38:41], v[100:103], v[18:21]
	v_mfma_f32_16x16x32_bf16 v[22:25], v[38:41], v[104:107], v[22:25]
	v_mfma_f32_16x16x32_bf16 v[26:29], v[38:41], v[108:111], v[26:29]
	v_mfma_f32_16x16x32_bf16 v[30:33], v[38:41], v[112:115], v[30:33]
	v_mfma_f32_16x16x32_bf16 v[34:37], v[38:41], v[116:119], v[34:37]
	s_waitcnt vmcnt(4)
	s_waitcnt lgkmcnt(0)
	s_barrier
	s_mov_b32 s33, s94
	s_mov_b32 s94, s95
	s_mov_b32 s95, s91
	s_mov_b32 s91, s25
	s_mov_b32 s25, s33
	v_add_u32_e32 v214, s95, v212
	v_add_u32_e32 v215, s95, v213
	ds_read_b128 v[38:41], v215
	ds_read_b128 v[58:61], v214 offset:0
	ds_read_b128 v[62:65], v214 offset:2048
	ds_read_b128 v[66:69], v214 offset:4096
	ds_read_b128 v[70:73], v214 offset:6144
	ds_read_b128 v[74:77], v214 offset:8192
	ds_read_b128 v[100:103], v214 offset:10240
	ds_read_b128 v[104:107], v214 offset:12288
	ds_read_b128 v[108:111], v214 offset:14336
	ds_read_b128 v[112:115], v214 offset:16384
	ds_read_b128 v[116:119], v214 offset:18432
	v_mfma_f32_16x16x32_bf16 v[18:21], v[226:229], v[230:233], v[18:21]
	v_mfma_f32_16x16x32_bf16 v[22:25], v[226:229], v[234:237], v[22:25]
	v_mfma_f32_16x16x32_bf16 v[26:29], v[226:229], v[238:241], v[26:29]
	v_mfma_f32_16x16x32_bf16 v[30:33], v[226:229], v[242:245], v[30:33]
	v_mfma_f32_16x16x32_bf16 v[34:37], v[226:229], v[246:249], v[34:37]
	v_mfma_f32_16x16x32_bf16 v[42:45], v[226:229], v[226:229], v[42:45]
	v_mfma_f32_16x16x32_bf16 v[18:21], v[226:229], v[120:123], v[18:21]
	v_mfma_f32_16x16x32_bf16 v[22:25], v[226:229], v[124:127], v[22:25]
	v_mfma_f32_16x16x32_bf16 v[26:29], v[226:229], v[132:135], v[26:29]
	v_mfma_f32_16x16x32_bf16 v[30:33], v[226:229], v[136:139], v[30:33]
	v_mfma_f32_16x16x32_bf16 v[34:37], v[226:229], v[140:143], v[34:37]
	s_waitcnt vmcnt(0)
	s_waitcnt lgkmcnt(0)
	s_barrier
	s_mov_b32 s33, s94
	s_mov_b32 s94, s95
	s_mov_b32 s95, s91
	s_mov_b32 s91, s25
	s_mov_b32 s25, s33
	v_add_u32_e32 v214, s95, v212
	v_add_u32_e32 v215, s95, v213
	ds_read_b128 v[226:229], v215
	ds_read_b128 v[230:233], v214 offset:0
	ds_read_b128 v[234:237], v214 offset:2048
	ds_read_b128 v[238:241], v214 offset:4096
	ds_read_b128 v[242:245], v214 offset:6144
	ds_read_b128 v[246:249], v214 offset:8192
	ds_read_b128 v[120:123], v214 offset:10240
	ds_read_b128 v[124:127], v214 offset:12288
	ds_read_b128 v[132:135], v214 offset:14336
	ds_read_b128 v[136:139], v214 offset:16384
	ds_read_b128 v[140:143], v214 offset:18432
	v_mfma_f32_16x16x32_bf16 v[18:21], v[38:41], v[58:61], v[18:21]
	v_mfma_f32_16x16x32_bf16 v[22:25], v[38:41], v[62:65], v[22:25]
	v_mfma_f32_16x16x32_bf16 v[26:29], v[38:41], v[66:69], v[26:29]
	v_mfma_f32_16x16x32_bf16 v[30:33], v[38:41], v[70:73], v[30:33]
	v_mfma_f32_16x16x32_bf16 v[34:37], v[38:41], v[74:77], v[34:37]
	v_mfma_f32_16x16x32_bf16 v[42:45], v[38:41], v[38:41], v[42:45]
	v_mfma_f32_16x16x32_bf16 v[18:21], v[38:41], v[100:103], v[18:21]
	v_mfma_f32_16x16x32_bf16 v[22:25], v[38:41], v[104:107], v[22:25]
	v_mfma_f32_16x16x32_bf16 v[26:29], v[38:41], v[108:111], v[26:29]
	v_mfma_f32_16x16x32_bf16 v[30:33], v[38:41], v[112:115], v[30:33]
	v_mfma_f32_16x16x32_bf16 v[34:37], v[38:41], v[116:119], v[34:37]
	s_waitcnt lgkmcnt(0)
	s_barrier
	s_mov_b32 s33, s94
	s_mov_b32 s94, s95
	s_mov_b32 s95, s91
	s_mov_b32 s91, s25
	s_mov_b32 s25, s33
	v_mfma_f32_16x16x32_bf16 v[18:21], v[226:229], v[230:233], v[18:21]
	v_mfma_f32_16x16x32_bf16 v[22:25], v[226:229], v[234:237], v[22:25]
	v_mfma_f32_16x16x32_bf16 v[26:29], v[226:229], v[238:241], v[26:29]
	v_mfma_f32_16x16x32_bf16 v[30:33], v[226:229], v[242:245], v[30:33]
	v_mfma_f32_16x16x32_bf16 v[34:37], v[226:229], v[246:249], v[34:37]
	v_mfma_f32_16x16x32_bf16 v[42:45], v[226:229], v[226:229], v[42:45]
	v_mfma_f32_16x16x32_bf16 v[18:21], v[226:229], v[120:123], v[18:21]
	v_mfma_f32_16x16x32_bf16 v[22:25], v[226:229], v[124:127], v[22:25]
	v_mfma_f32_16x16x32_bf16 v[26:29], v[226:229], v[132:135], v[26:29]
	v_mfma_f32_16x16x32_bf16 v[30:33], v[226:229], v[136:139], v[30:33]
	v_mfma_f32_16x16x32_bf16 v[34:37], v[226:229], v[140:143], v[34:37]
	s_branch .Lrt_out
; __device__ __forceinline__ void rt_step(const RtLoad& L, const bf16_t* bh, const bf16_t* bl, f32x4 (&acc)[2][5], float (&ss)[2], int ko) {
;     RtW W;
; #pragma unroll
;     for (int n = 0; n < 5; ++n) { W.wh[n] = *(const bf16x8*)(bh + (size_t)n * 16 * D + ko); W.wl[n] = *(const bf16x8*)(bl + (size_t)n * 16 * D + ko); }
;     bf16x8 ahi[2], alo[2];
; #pragma unroll
;     for (int mi = 0; mi < 2; ++mi) { const u32x4 xw = L.x[mi]; const f32x4 xa = (f32x4){bflo(xw.x), bfhi(xw.x), bflo(xw.y), bfhi(xw.y)}, xb = (f32x4){bflo(xw.z), bfhi(xw.z), bflo(xw.w), bfhi(xw.w)};
;         ss[mi] += (xa.x * xa.x + xa.y * xa.y) + (xa.z * xa.z + xa.w * xa.w) + (xb.x * xb.x + xb.y * xb.y) + (xb.z * xb.z + xb.w * xb.w);
;         const float u[8] = {xa.x * L.g[0].x, xa.y * L.g[0].y, xa.z * L.g[0].z, xa.w * L.g[0].w, xb.x * L.g[1].x, xb.y * L.g[1].y, xb.z * L.g[1].z, xb.w * L.g[1].w};
;         unsigned hb[8]; float lo[8];
; #pragma unroll
;         for (int j = 0; j < 8; ++j) { hb[j] = f2bf(u[j]); lo[j] = u[j] - __builtin_bit_cast(float, hb[j] << 16); }
;         const u32x4 hw = (u32x4){hb[0] | (hb[1] << 16), hb[2] | (hb[3] << 16), hb[4] | (hb[5] << 16), hb[6] | (hb[7] << 16)};
;         const u32x4 lw = (u32x4){pk2(lo[0], lo[1]), pk2(lo[2], lo[3]), pk2(lo[4], lo[5]), pk2(lo[6], lo[7])};
; __device__ __forceinline__ void p5_router(Frame& F) {
;     ...
;         { const int tg = wave & 1, kq = wave >> 1, fr = lane & 15, fq = lane >> 4;
;           f32x4 acc[2][5];
; #pragma unroll
;           for (int a = 0; a < 2; ++a)
; #pragma unroll
;               for (int n = 0; n < 5; ++n) acc[a][n] = (f32x4){0.f, 0.f, 0.f, 0.f};
;           float ss[2] = {0.f, 0.f};
;           const size_t roff = (size_t)(m0 + 32 * tg + fr) * D + kq * 1024 + 8 * fq;
;           const bf16_t* h0 = H + roff; const bf16_t* h1 = h0 + (size_t)16 * D;
;           const float* gp = F.g_ffn + kq * 1024 + 8 * fq;
;           const bf16_t* bh = RBH + (size_t)fr * D + kq * 1024 + 8 * fq; const bf16_t* bl = RBL + (size_t)fr * D + kq * 1024 + 8 * fq;
;           RtLoad La, Lb; rt_load(La, h0, h1, gp, 0);
; #pragma unroll 1
;           for (int ks = 0; ks < 32; ks += 2) {
;               rt_load(Lb, h0, h1, gp, (ks + 1) * 32); rt_step(La, bh, bl, acc, ss, ks * 32);
;               if (ks + 2 < 32) rt_load(La, h0, h1, gp, (ks + 2) * 32);
;               rt_step(Lb, bh, bl, acc, ss, (ks + 1) * 32); }
.Lrt_path3:
	s_add_i32 s39, s39, 0x80
	s_and_b32 s39, s39, 0x1fff
	s_add_u32 s40, s86, s39
	s_addc_u32 s41, s87, 0
	s_add_i32 m0, s94, s98
	s_nop 0
	global_load_lds_dwordx4 v208, s[40:41]
	s_add_i32 m0, s94, s99
	s_nop 0
	global_load_lds_dwordx4 v209, s[40:41]
	s_add_i32 m0, s94, s100
	s_nop 0
	global_load_lds_dwordx4 v210, s[40:41]
	v_add_u32_e32 v214, s95, v212
	v_add_u32_e32 v215, s95, v213
	ds_read_b128 v[38:41], v215
	ds_read_b128 v[58:61], v214 offset:0
	ds_read_b128 v[62:65], v214 offset:2048
	ds_read_b128 v[66:69], v214 offset:4096
	ds_read_b128 v[70:73], v214 offset:6144
	ds_read_b128 v[74:77], v214 offset:8192
	ds_read_b128 v[100:103], v214 offset:10240
	ds_read_b128 v[104:107], v214 offset:12288
	ds_read_b128 v[108:111], v214 offset:14336
	ds_read_b128 v[112:115], v214 offset:16384
	ds_read_b128 v[116:119], v214 offset:18432
	s_waitcnt vmcnt(6)
	s_waitcnt lgkmcnt(0)
	s_barrier
	s_mov_b32 s33, s94
	s_mov_b32 s94, s95
	s_mov_b32 s95, s91
	s_mov_b32 s91, s25
	s_mov_b32 s25, s33
	s_add_i32 s39, s39, 0x80
	s_and_b32 s39, s39, 0x1fff
	s_add_u32 s40, s86, s39
	s_addc_u32 s41, s87, 0
	s_add_i32 m0, s94, s98
	s_nop 0
	global_load_lds_dwordx4 v208, s[40:41]
	s_add_i32 m0, s94, s99
	s_nop 0
	global_load_lds_dwordx4 v209, s[40:41]
	s_add_i32 m0, s94, s100
	s_nop 0
	global_load_lds_dwordx4 v210, s[40:41]
	v_add_u32_e32 v214, s95, v212
	v_add_u32_e32 v215, s95, v213
	ds_read_b128 v[226:229], v215
	ds_read_b128 v[230:233], v214 offset:0
	ds_read_b128 v[234:237], v214 offset:2048
	ds_read_b128 v[238:241], v214 offset:4096
	ds_read_b128 v[242:245], v214 offset:6144
	ds_read_b128 v[246:249], v214 offset:8192
	ds_read_b128 v[120:123], v214 offset:10240
	ds_read_b128 v[124:127], v214 offset:12288
	ds_read_b128 v[132:135], v214 offset:14336
	ds_read_b128 v[136:139], v214 offset:16384
	ds_read_b128 v[140:143], v214 offset:18432
	v_mfma_f32_16x16x32_bf16 v[18:21], v[38:41], v[58:61], v[18:21]
	v_mfma_f32_16x16x32_bf16 v[22:25], v[38:41], v[62:65], v[22:25]
	v_mfma_f32_16x16x32_bf16 v[26:29], v[38:41], v[66:69], v[26:29]
	v_mfma_f32_16x16x32_bf16 v[30:33], v[38:41], v[70:73], v[30:33]
	v_mfma_f32_16x16x32_bf16 v[34:37], v[38:41], v[74:77], v[34:37]
	v_mfma_f32_16x16x32_bf16 v[42:45], v[38:41], v[38:41], v[42:45]
	v_mfma_f32_16x16x32_bf16 v[18:21], v[38:41], v[100:103], v[18:21]
	v_mfma_f32_16x16x32_bf16 v[22:25], v[38:41], v[104:107], v[22:25]
	v_mfma_f32_16x16x32_bf16 v[26:29], v[38:41], v[108:111], v[26:29]
	v_mfma_f32_16x16x32_bf16 v[30:33], v[38:41], v[112:115], v[30:33]
	v_mfma_f32_16x16x32_bf16 v[34:37], v[38:41], v[116:119], v[34:37]
	s_waitcnt vmcnt(6)
	s_waitcnt lgkmcnt(0)
	s_barrier
	s_mov_b32 s33, s94
	s_mov_b32 s94, s95
	s_mov_b32 s95, s91
	s_mov_b32 s91, s25
	s_mov_b32 s25, s33
	s_add_i32 s39, s39, 0x80
	s_and_b32 s39, s39, 0x1fff
	s_add_u32 s40, s86, s39
	s_addc_u32 s41, s87, 0
	s_add_i32 m0, s94, s98
	s_nop 0
	global_load_lds_dwordx4 v208, s[40:41]
	s_add_i32 m0, s94, s99
	s_nop 0
	global_load_lds_dwordx4 v209, s[40:41]
	s_add_i32 m0, s94, s100
	s_nop 0
	global_load_lds_dwordx4 v210, s[40:41]
	v_add_u32_e32 v214, s95, v212
	v_add_u32_e32 v215, s95, v213
	ds_read_b128 v[38:41], v215
	ds_read_b128 v[58:61], v214 offset:0
	ds_read_b128 v[62:65], v214 offset:2048
	ds_read_b128 v[66:69], v214 offset:4096
	ds_read_b128 v[70:73], v214 offset:6144
	ds_read_b128 v[74:77], v214 offset:8192
	ds_read_b128 v[100:103], v214 offset:10240
	ds_read_b128 v[104:107], v214 offset:12288
	ds_read_b128 v[108:111], v214 offset:14336
	ds_read_b128 v[112:115], v214 offset:16384
	ds_read_b128 v[116:119], v214 offset:18432
	v_mfma_f32_16x16x32_bf16 v[18:21], v[226:229], v[230:233], v[18:21]
	v_mfma_f32_16x16x32_bf16 v[22:25], v[226:229], v[234:237], v[22:25]
	v_mfma_f32_16x16x32_bf16 v[26:29], v[226:229], v[238:241], v[26:29]
	v_mfma_f32_16x16x32_bf16 v[30:33], v[226:229], v[242:245], v[30:33]
	v_mfma_f32_16x16x32_bf16 v[34:37], v[226:229], v[246:249], v[34:37]
	v_mfma_f32_16x16x32_bf16 v[42:45], v[226:229], v[226:229], v[42:45]
	v_mfma_f32_16x16x32_bf16 v[18:21], v[226:229], v[120:123], v[18:21]
	v_mfma_f32_16x16x32_bf16 v[22:25], v[226:229], v[124:127], v[22:25]
	v_mfma_f32_16x16x32_bf16 v[26:29], v[226:229], v[132:135], v[26:29]
	v_mfma_f32_16x16x32_bf16 v[30:33], v[226:229], v[136:139], v[30:33]
	v_mfma_f32_16x16x32_bf16 v[34:37], v[226:229], v[140:143], v[34:37]
	s_waitcnt vmcnt(6)
	s_waitcnt lgkmcnt(0)
	s_barrier
	s_mov_b32 s33, s94
	s_mov_b32 s94, s95
	s_mov_b32 s95, s91
	s_mov_b32 s91, s25
	s_mov_b32 s25, s33
	s_add_i32 s39, s39, 0x80
	s_and_b32 s39, s39, 0x1fff
	s_add_u32 s40, s86, s39
	s_addc_u32 s41, s87, 0
	s_add_i32 m0, s94, s98
	s_nop 0
	global_load_lds_dwordx4 v208, s[40:41]
	s_add_i32 m0, s94, s99
	s_nop 0
	global_load_lds_dwordx4 v209, s[40:41]
	s_add_i32 m0, s94, s100
	s_nop 0
	global_load_lds_dwordx4 v210, s[40:41]
	v_add_u32_e32 v214, s95, v212
	v_add_u32_e32 v215, s95, v213
	ds_read_b128 v[226:229], v215
	ds_read_b128 v[230:233], v214 offset:0
	ds_read_b128 v[234:237], v214 offset:2048
	ds_read_b128 v[238:241], v214 offset:4096
	ds_read_b128 v[242:245], v214 offset:6144
	ds_read_b128 v[246:249], v214 offset:8192
	ds_read_b128 v[120:123], v214 offset:10240
	ds_read_b128 v[124:127], v214 offset:12288
	ds_read_b128 v[132:135], v214 offset:14336
	ds_read_b128 v[136:139], v214 offset:16384
	ds_read_b128 v[140:143], v214 offset:18432
	v_mfma_f32_16x16x32_bf16 v[18:21], v[38:41], v[58:61], v[18:21]
	v_mfma_f32_16x16x32_bf16 v[22:25], v[38:41], v[62:65], v[22:25]
	v_mfma_f32_16x16x32_bf16 v[26:29], v[38:41], v[66:69], v[26:29]
	v_mfma_f32_16x16x32_bf16 v[30:33], v[38:41], v[70:73], v[30:33]
	v_mfma_f32_16x16x32_bf16 v[34:37], v[38:41], v[74:77], v[34:37]
	v_mfma_f32_16x16x32_bf16 v[42:45], v[38:41], v[38:41], v[42:45]
	v_mfma_f32_16x16x32_bf16 v[18:21], v[38:41], v[100:103], v[18:21]
	v_mfma_f32_16x16x32_bf16 v[22:25], v[38:41], v[104:107], v[22:25]
	v_mfma_f32_16x16x32_bf16 v[26:29], v[38:41], v[108:111], v[26:29]
	v_mfma_f32_16x16x32_bf16 v[30:33], v[38:41], v[112:115], v[30:33]
	v_mfma_f32_16x16x32_bf16 v[34:37], v[38:41], v[116:119], v[34:37]
	s_waitcnt vmcnt(6)
	s_waitcnt lgkmcnt(0)
	s_barrier
; __device__ __forceinline__ void rt_step(const RtLoad& L, const bf16_t* bh, const bf16_t* bl, f32x4 (&acc)[2][5], float (&ss)[2], int ko) {
;     RtW W;
; #pragma unroll
;     for (int n = 0; n < 5; ++n) { W.wh[n] = *(const bf16x8*)(bh + (size_t)n * 16 * D + ko); W.wl[n] = *(const bf16x8*)(bl + (size_t)n * 16 * D + ko); }
;     bf16x8 ahi[2], alo[2];
; #pragma unroll
;     for (int mi = 0; mi < 2; ++mi) { const u32x4 xw = L.x[mi]; const f32x4 xa = (f32x4){bflo(xw.x), bfhi(xw.x), bflo(xw.y), bfhi(xw.y)}, xb = (f32x4){bflo(xw.z), bfhi(xw.z), bflo(xw.w), bfhi(xw.w)};
;         ss[mi] += (xa.x * xa.x + xa.y * xa.y) + (xa.z * xa.z + xa.w * xa.w) + (xb.x * xb.x + xb.y * xb.y) + (xb.z * xb.z + xb.w * xb.w);
;         const float u[8] = {xa.x * L.g[0].x, xa.y * L.g[0].y, xa.z * L.g[0].z, xa.w * L.g[0].w, xb.x * L.g[1].x, xb.y * L.g[1].y, xb.z * L.g[1].z, xb.w * L.g[1].w};
;         unsigned hb[8]; float lo[8];
; #pragma unroll
;         for (int j = 0; j < 8; ++j) { hb[j] = f2bf(u[j]); lo[j] = u[j] - __builtin_bit_cast(float, hb[j] << 16); }
;         const u32x4 hw = (u32x4){hb[0] | (hb[1] << 16), hb[2] | (hb[3] << 16), hb[4] | (hb[5] << 16), hb[6] | (hb[7] << 16)};
;         const u32x4 lw = (u32x4){pk2(lo[0], lo[1]), pk2(lo[2], lo[3]), pk2(lo[4], lo[5]), pk2(lo[6], lo[7])};
; __device__ __forceinline__ void p5_router(Frame& F) {
;     ...
;         { const int tg = wave & 1, kq = wave >> 1, fr = lane & 15, fq = lane >> 4;
;           f32x4 acc[2][5];
; #pragma unroll
;           for (int a = 0; a < 2; ++a)
; #pragma unroll
;               for (int n = 0; n < 5; ++n) acc[a][n] = (f32x4){0.f, 0.f, 0.f, 0.f};
;           float ss[2] = {0.f, 0.f};
;           const size_t roff = (size_t)(m0 + 32 * tg + fr) * D + kq * 1024 + 8 * fq;
;           const bf16_t* h0 = H + roff; const bf16_t* h1 = h0 + (size_t)16 * D;
;           const float* gp = F.g_ffn + kq * 1024 + 8 * fq;
;           const bf16_t* bh = RBH + (size_t)fr * D + kq * 1024 + 8 * fq; const bf16_t* bl = RBL + (size_t)fr * D + kq * 1024 + 8 * fq;
;           RtLoad La, Lb; rt_load(La, h0, h1, gp, 0);
; #pragma unroll 1
;           for (int ks = 0; ks < 32; ks += 2) {
;               rt_load(Lb, h0, h1, gp, (ks + 1) * 32); rt_step(La, bh, bl, acc, ss, ks * 32);
;               if (ks + 2 < 32) rt_load(La, h0, h1, gp, (ks + 2) * 32);
;               rt_step(Lb, bh, bl, acc, ss, (ks + 1) * 32); }
	s_mov_b32 s33, s94
	s_mov_b32 s94, s95
	s_mov_b32 s95, s91
	s_mov_b32 s91, s25
	s_mov_b32 s25, s33
	s_add_i32 s39, s39, 0x80
	s_and_b32 s39, s39, 0x1fff
	s_add_u32 s40, s86, s39
	s_addc_u32 s41, s87, 0
	s_add_i32 m0, s94, s98
	s_nop 0
	global_load_lds_dwordx4 v208, s[40:41]
	s_add_i32 m0, s94, s99
	s_nop 0
	global_load_lds_dwordx4 v209, s[40:41]
	s_add_i32 m0, s94, s100
	s_nop 0
	global_load_lds_dwordx4 v210, s[40:41]
	v_add_u32_e32 v214, s95, v212
	v_add_u32_e32 v215, s95, v213
	ds_read_b128 v[38:41], v215
	ds_read_b128 v[58:61], v214 offset:0
	ds_read_b128 v[62:65], v214 offset:2048
	ds_read_b128 v[66:69], v214 offset:4096
	ds_read_b128 v[70:73], v214 offset:6144
	ds_read_b128 v[74:77], v214 offset:8192
	ds_read_b128 v[100:103], v214 offset:10240
	ds_read_b128 v[104:107], v214 offset:12288
	ds_read_b128 v[108:111], v214 offset:14336
	ds_read_b128 v[112:115], v214 offset:16384
	ds_read_b128 v[116:119], v214 offset:18432
	v_mfma_f32_16x16x32_bf16 v[18:21], v[226:229], v[230:233], v[18:21]
	v_mfma_f32_16x16x32_bf16 v[22:25], v[226:229], v[234:237], v[22:25]
	v_mfma_f32_16x16x32_bf16 v[26:29], v[226:229], v[238:241], v[26:29]
	v_mfma_f32_16x16x32_bf16 v[30:33], v[226:229], v[242:245], v[30:33]
	v_mfma_f32_16x16x32_bf16 v[34:37], v[226:229], v[246:249], v[34:37]
	v_mfma_f32_16x16x32_bf16 v[42:45], v[226:229], v[226:229], v[42:45]
	v_mfma_f32_16x16x32_bf16 v[18:21], v[226:229], v[120:123], v[18:21]
	v_mfma_f32_16x16x32_bf16 v[22:25], v[226:229], v[124:127], v[22:25]
	v_mfma_f32_16x16x32_bf16 v[26:29], v[226:229], v[132:135], v[26:29]
	v_mfma_f32_16x16x32_bf16 v[30:33], v[226:229], v[136:139], v[30:33]
	v_mfma_f32_16x16x32_bf16 v[34:37], v[226:229], v[140:143], v[34:37]
	s_waitcnt vmcnt(6)
	s_waitcnt lgkmcnt(0)
	s_barrier
	s_mov_b32 s33, s94
	s_mov_b32 s94, s95
	s_mov_b32 s95, s91
	s_mov_b32 s91, s25
	s_mov_b32 s25, s33
	s_mov_b32 s85, 13
.Lrt_loop_p3:
	s_add_i32 s39, s39, 0x80
	s_and_b32 s39, s39, 0x1fff
	s_add_u32 s40, s86, s39
	s_addc_u32 s41, s87, 0
	s_add_i32 m0, s94, s98
	s_nop 0
	global_load_lds_dwordx4 v208, s[40:41]
	s_add_i32 m0, s94, s99
	s_nop 0
	global_load_lds_dwordx4 v209, s[40:41]
	s_add_i32 m0, s94, s100
	s_nop 0
	global_load_lds_dwordx4 v210, s[40:41]
	v_add_u32_e32 v214, s95, v212
	v_add_u32_e32 v215, s95, v213
	ds_read_b128 v[226:229], v215
	ds_read_b128 v[230:233], v214 offset:0
	ds_read_b128 v[234:237], v214 offset:2048
	ds_read_b128 v[238:241], v214 offset:4096
	ds_read_b128 v[242:245], v214 offset:6144
	ds_read_b128 v[246:249], v214 offset:8192
	ds_read_b128 v[120:123], v214 offset:10240
	ds_read_b128 v[124:127], v214 offset:12288
	ds_read_b128 v[132:135], v214 offset:14336
	ds_read_b128 v[136:139], v214 offset:16384
	ds_read_b128 v[140:143], v214 offset:18432
	v_mfma_f32_16x16x32_bf16 v[18:21], v[38:41], v[58:61], v[18:21]
	v_mfma_f32_16x16x32_bf16 v[22:25], v[38:41], v[62:65], v[22:25]
	v_mfma_f32_16x16x32_bf16 v[26:29], v[38:41], v[66:69], v[26:29]
	v_mfma_f32_16x16x32_bf16 v[30:33], v[38:41], v[70:73], v[30:33]
	v_mfma_f32_16x16x32_bf16 v[34:37], v[38:41], v[74:77], v[34:37]
	v_mfma_f32_16x16x32_bf16 v[42:45], v[38:41], v[38:41], v[42:45]
	v_mfma_f32_16x16x32_bf16 v[18:21], v[38:41], v[100:103], v[18:21]
	v_mfma_f32_16x16x32_bf16 v[22:25], v[38:41], v[104:107], v[22:25]
	v_mfma_f32_16x16x32_bf16 v[26:29], v[38:41], v[108:111], v[26:29]
	v_mfma_f32_16x16x32_bf16 v[30:33], v[38:41], v[112:115], v[30:33]
	v_mfma_f32_16x16x32_bf16 v[34:37], v[38:41], v[116:119], v[34:37]
	s_waitcnt vmcnt(6)
	s_waitcnt lgkmcnt(0)
	s_barrier
	s_mov_b32 s33, s94
	s_mov_b32 s94, s95
	s_mov_b32 s95, s91
	s_mov_b32 s91, s25
	s_mov_b32 s25, s33
	s_add_i32 s39, s39, 0x80
	s_and_b32 s39, s39, 0x1fff
	s_add_u32 s40, s86, s39
	s_addc_u32 s41, s87, 0
	s_add_i32 m0, s94, s98
	s_nop 0
	global_load_lds_dwordx4 v208, s[40:41]
	s_add_i32 m0, s94, s99
	s_nop 0
	global_load_lds_dwordx4 v209, s[40:41]
	s_add_i32 m0, s94, s100
	s_nop 0
	global_load_lds_dwordx4 v210, s[40:41]
	v_add_u32_e32 v214, s95, v212
	v_add_u32_e32 v215, s95, v213
	ds_read_b128 v[38:41], v215
	ds_read_b128 v[58:61], v214 offset:0
	ds_read_b128 v[62:65], v214 offset:2048
	ds_read_b128 v[66:69], v214 offset:4096
	ds_read_b128 v[70:73], v214 offset:6144
	ds_read_b128 v[74:77], v214 offset:8192
	ds_read_b128 v[100:103], v214 offset:10240
	ds_read_b128 v[104:107], v214 offset:12288
	ds_read_b128 v[108:111], v214 offset:14336
	ds_read_b128 v[112:115], v214 offset:16384
	ds_read_b128 v[116:119], v214 offset:18432
	v_mfma_f32_16x16x32_bf16 v[18:21], v[226:229], v[230:233], v[18:21]
	v_mfma_f32_16x16x32_bf16 v[22:25], v[226:229], v[234:237], v[22:25]
	v_mfma_f32_16x16x32_bf16 v[26:29], v[226:229], v[238:241], v[26:29]
	v_mfma_f32_16x16x32_bf16 v[30:33], v[226:229], v[242:245], v[30:33]
	v_mfma_f32_16x16x32_bf16 v[34:37], v[226:229], v[246:249], v[34:37]
	v_mfma_f32_16x16x32_bf16 v[42:45], v[226:229], v[226:229], v[42:45]
	v_mfma_f32_16x16x32_bf16 v[18:21], v[226:229], v[120:123], v[18:21]
	v_mfma_f32_16x16x32_bf16 v[22:25], v[226:229], v[124:127], v[22:25]
	v_mfma_f32_16x16x32_bf16 v[26:29], v[226:229], v[132:135], v[26:29]
	v_mfma_f32_16x16x32_bf16 v[30:33], v[226:229], v[136:139], v[30:33]
	v_mfma_f32_16x16x32_bf16 v[34:37], v[226:229], v[140:143], v[34:37]
	s_waitcnt vmcnt(6)
	s_waitcnt lgkmcnt(0)
	s_barrier
; __device__ __forceinline__ void rt_step(const RtLoad& L, const bf16_t* bh, const bf16_t* bl, f32x4 (&acc)[2][5], float (&ss)[2], int ko) {
;     RtW W;
; #pragma unroll
;     for (int n = 0; n < 5; ++n) { W.wh[n] = *(const bf16x8*)(bh + (size_t)n * 16 * D + ko); W.wl[n] = *(const bf16x8*)(bl + (size_t)n * 16 * D + ko); }
;     bf16x8 ahi[2], alo[2];
; #pragma unroll
;     for (int mi = 0; mi < 2; ++mi) { const u32x4 xw = L.x[mi]; const f32x4 xa = (f32x4){bflo(xw.x), bfhi(xw.x), bflo(xw.y), bfhi(xw.y)}, xb = (f32x4){bflo(xw.z), bfhi(xw.z), bflo(xw.w), bfhi(xw.w)};
;         ss[mi] += (xa.x * xa.x + xa.y * xa.y) + (xa.z * xa.z + xa.w * xa.w) + (xb.x * xb.x + xb.y * xb.y) + (xb.z * xb.z + xb.w * xb.w);
;         const float u[8] = {xa.x * L.g[0].x, xa.y * L.g[0].y, xa.z * L.g[0].z, xa.w * L.g[0].w, xb.x * L.g[1].x, xb.y * L.g[1].y, xb.z * L.g[1].z, xb.w * L.g[1].w};
;         unsigned hb[8]; float lo[8];
; #pragma unroll
;         for (int j = 0; j < 8; ++j) { hb[j] = f2bf(u[j]); lo[j] = u[j] - __builtin_bit_cast(float, hb[j] << 16); }
;         const u32x4 hw = (u32x4){hb[0] | (hb[1] << 16), hb[2] | (hb[3] << 16), hb[4] | (hb[5] << 16), hb[6] | (hb[7] << 16)};
;         const u32x4 lw = (u32x4){pk2(lo[0], lo[1]), pk2(lo[2], lo[3]), pk2(lo[4], lo[5]), pk2(lo[6], lo[7])};
; __device__ __forceinline__ void p5_router(Frame& F) {
;     ...
;         { const int tg = wave & 1, kq = wave >> 1, fr = lane & 15, fq = lane >> 4;
;           f32x4 acc[2][5];
; #pragma unroll
;           for (int a = 0; a < 2; ++a)
; #pragma unroll
;               for (int n = 0; n < 5; ++n) acc[a][n] = (f32x4){0.f, 0.f, 0.f, 0.f};
;           float ss[2] = {0.f, 0.f};
;           const size_t roff = (size_t)(m0 + 32 * tg + fr) * D + kq * 1024 + 8 * fq;
;           const bf16_t* h0 = H + roff; const bf16_t* h1 = h0 + (size_t)16 * D;
;           const float* gp = F.g_ffn + kq * 1024 + 8 * fq;
;           const bf16_t* bh = RBH + (size_t)fr * D + kq * 1024 + 8 * fq; const bf16_t* bl = RBL + (size_t)fr * D + kq * 1024 + 8 * fq;
;           RtLoad La, Lb; rt_load(La, h0, h1, gp, 0);
; #pragma unroll 1
;           for (int ks = 0; ks < 32; ks += 2) {
;               rt_load(Lb, h0, h1, gp, (ks + 1) * 32); rt_step(La, bh, bl, acc, ss, ks * 32);
;               if (ks + 2 < 32) rt_load(La, h0, h1, gp, (ks + 2) * 32);
;               rt_step(Lb, bh, bl, acc, ss, (ks + 1) * 32); }
	s_mov_b32 s33, s94
	s_mov_b32 s94, s95
	s_mov_b32 s95, s91
	s_mov_b32 s91, s25
	s_mov_b32 s25, s33
	s_add_i32 s39, s39, 0x80
	s_and_b32 s39, s39, 0x1fff
	s_add_u32 s40, s86, s39
	s_addc_u32 s41, s87, 0
	s_add_i32 m0, s94, s98
	s_nop 0
	global_load_lds_dwordx4 v208, s[40:41]
	s_add_i32 m0, s94, s99
	s_nop 0
	global_load_lds_dwordx4 v209, s[40:41]
	s_add_i32 m0, s94, s100
	s_nop 0
	global_load_lds_dwordx4 v210, s[40:41]
	v_add_u32_e32 v214, s95, v212
	v_add_u32_e32 v215, s95, v213
	ds_read_b128 v[226:229], v215
	ds_read_b128 v[230:233], v214 offset:0
	ds_read_b128 v[234:237], v214 offset:2048
	ds_read_b128 v[238:241], v214 offset:4096
	ds_read_b128 v[242:245], v214 offset:6144
	ds_read_b128 v[246:249], v214 offset:8192
	ds_read_b128 v[120:123], v214 offset:10240
	ds_read_b128 v[124:127], v214 offset:12288
	ds_read_b128 v[132:135], v214 offset:14336
	ds_read_b128 v[136:139], v214 offset:16384
	ds_read_b128 v[140:143], v214 offset:18432
	v_mfma_f32_16x16x32_bf16 v[18:21], v[38:41], v[58:61], v[18:21]
	v_mfma_f32_16x16x32_bf16 v[22:25], v[38:41], v[62:65], v[22:25]
	v_mfma_f32_16x16x32_bf16 v[26:29], v[38:41], v[66:69], v[26:29]
	v_mfma_f32_16x16x32_bf16 v[30:33], v[38:41], v[70:73], v[30:33]
	v_mfma_f32_16x16x32_bf16 v[34:37], v[38:41], v[74:77], v[34:37]
	v_mfma_f32_16x16x32_bf16 v[42:45], v[38:41], v[38:41], v[42:45]
	v_mfma_f32_16x16x32_bf16 v[18:21], v[38:41], v[100:103], v[18:21]
	v_mfma_f32_16x16x32_bf16 v[22:25], v[38:41], v[104:107], v[22:25]
	v_mfma_f32_16x16x32_bf16 v[26:29], v[38:41], v[108:111], v[26:29]
	v_mfma_f32_16x16x32_bf16 v[30:33], v[38:41], v[112:115], v[30:33]
	v_mfma_f32_16x16x32_bf16 v[34:37], v[38:41], v[116:119], v[34:37]
	s_waitcnt vmcnt(6)
	s_waitcnt lgkmcnt(0)
	s_barrier
	s_mov_b32 s33, s94
	s_mov_b32 s94, s95
	s_mov_b32 s95, s91
	s_mov_b32 s91, s25
	s_mov_b32 s25, s33
	s_add_i32 s39, s39, 0x80
	s_and_b32 s39, s39, 0x1fff
	s_add_u32 s40, s86, s39
	s_addc_u32 s41, s87, 0
	s_add_i32 m0, s94, s98
	s_nop 0
	global_load_lds_dwordx4 v208, s[40:41]
	s_add_i32 m0, s94, s99
	s_nop 0
	global_load_lds_dwordx4 v209, s[40:41]
	s_add_i32 m0, s94, s100
	s_nop 0
	global_load_lds_dwordx4 v210, s[40:41]
	v_add_u32_e32 v214, s95, v212
	v_add_u32_e32 v215, s95, v213
	ds_read_b128 v[38:41], v215
	ds_read_b128 v[58:61], v214 offset:0
	ds_read_b128 v[62:65], v214 offset:2048
	ds_read_b128 v[66:69], v214 offset:4096
	ds_read_b128 v[70:73], v214 offset:6144
	ds_read_b128 v[74:77], v214 offset:8192
	ds_read_b128 v[100:103], v214 offset:10240
	ds_read_b128 v[104:107], v214 offset:12288
	ds_read_b128 v[108:111], v214 offset:14336
	ds_read_b128 v[112:115], v214 offset:16384
	ds_read_b128 v[116:119], v214 offset:18432
	v_mfma_f32_16x16x32_bf16 v[18:21], v[226:229], v[230:233], v[18:21]
	v_mfma_f32_16x16x32_bf16 v[22:25], v[226:229], v[234:237], v[22:25]
	v_mfma_f32_16x16x32_bf16 v[26:29], v[226:229], v[238:241], v[26:29]
	v_mfma_f32_16x16x32_bf16 v[30:33], v[226:229], v[242:245], v[30:33]
	v_mfma_f32_16x16x32_bf16 v[34:37], v[226:229], v[246:249], v[34:37]
	v_mfma_f32_16x16x32_bf16 v[42:45], v[226:229], v[226:229], v[42:45]
	v_mfma_f32_16x16x32_bf16 v[18:21], v[226:229], v[120:123], v[18:21]
	v_mfma_f32_16x16x32_bf16 v[22:25], v[226:229], v[124:127], v[22:25]
	v_mfma_f32_16x16x32_bf16 v[26:29], v[226:229], v[132:135], v[26:29]
	v_mfma_f32_16x16x32_bf16 v[30:33], v[226:229], v[136:139], v[30:33]
	v_mfma_f32_16x16x32_bf16 v[34:37], v[226:229], v[140:143], v[34:37]
	s_waitcnt vmcnt(6)
	s_waitcnt lgkmcnt(0)
	s_barrier
	s_mov_b32 s33, s94
	s_mov_b32 s94, s95
	s_mov_b32 s95, s91
	s_mov_b32 s91, s25
	s_mov_b32 s25, s33
	s_sub_u32 s85, s85, 1
	s_cmp_lg_u32 s85, 0
	s_cbranch_scc1 .Lrt_loop_p3
	s_add_i32 s39, s39, 0x80
	s_and_b32 s39, s39, 0x1fff
	s_add_u32 s40, s86, s39
	s_addc_u32 s41, s87, 0
	s_add_i32 m0, s94, s98
	s_nop 0
	global_load_lds_dwordx4 v208, s[40:41]
	s_add_i32 m0, s94, s99
	s_nop 0
	global_load_lds_dwordx4 v209, s[40:41]
	s_add_i32 m0, s94, s100
	s_nop 0
	global_load_lds_dwordx4 v210, s[40:41]
	v_add_u32_e32 v214, s95, v212
	v_add_u32_e32 v215, s95, v213
	ds_read_b128 v[226:229], v215
	ds_read_b128 v[230:233], v214 offset:0
	ds_read_b128 v[234:237], v214 offset:2048
	ds_read_b128 v[238:241], v214 offset:4096
	ds_read_b128 v[242:245], v214 offset:6144
	ds_read_b128 v[246:249], v214 offset:8192
	ds_read_b128 v[120:123], v214 offset:10240
	ds_read_b128 v[124:127], v214 offset:12288
	ds_read_b128 v[132:135], v214 offset:14336
	ds_read_b128 v[136:139], v214 offset:16384
	ds_read_b128 v[140:143], v214 offset:18432
	v_mfma_f32_16x16x32_bf16 v[18:21], v[38:41], v[58:61], v[18:21]
	v_mfma_f32_16x16x32_bf16 v[22:25], v[38:41], v[62:65], v[22:25]
	v_mfma_f32_16x16x32_bf16 v[26:29], v[38:41], v[66:69], v[26:29]
	v_mfma_f32_16x16x32_bf16 v[30:33], v[38:41], v[70:73], v[30:33]
	v_mfma_f32_16x16x32_bf16 v[34:37], v[38:41], v[74:77], v[34:37]
	v_mfma_f32_16x16x32_bf16 v[42:45], v[38:41], v[38:41], v[42:45]
	v_mfma_f32_16x16x32_bf16 v[18:21], v[38:41], v[100:103], v[18:21]
	v_mfma_f32_16x16x32_bf16 v[22:25], v[38:41], v[104:107], v[22:25]
	v_mfma_f32_16x16x32_bf16 v[26:29], v[38:41], v[108:111], v[26:29]
	v_mfma_f32_16x16x32_bf16 v[30:33], v[38:41], v[112:115], v[30:33]
	v_mfma_f32_16x16x32_bf16 v[34:37], v[38:41], v[116:119], v[34:37]
	s_waitcnt vmcnt(6)
	s_waitcnt lgkmcnt(0)
	s_barrier
; __device__ __forceinline__ void rt_step(const RtLoad& L, const bf16_t* bh, const bf16_t* bl, f32x4 (&acc)[2][5], float (&ss)[2], int ko) {
;     RtW W;
; #pragma unroll
;     for (int n = 0; n < 5; ++n) { W.wh[n] = *(const bf16x8*)(bh + (size_t)n * 16 * D + ko); W.wl[n] = *(const bf16x8*)(bl + (size_t)n * 16 * D + ko); }
;     bf16x8 ahi[2], alo[2];
; #pragma unroll
;     for (int mi = 0; mi < 2; ++mi) { const u32x4 xw = L.x[mi]; const f32x4 xa = (f32x4){bflo(xw.x), bfhi(xw.x), bflo(xw.y), bfhi(xw.y)}, xb = (f32x4){bflo(xw.z), bfhi(xw.z), bflo(xw.w), bfhi(xw.w)};
;         ss[mi] += (xa.x * xa.x + xa.y * xa.y) + (xa.z * xa.z + xa.w * xa.w) + (xb.x * xb.x + xb.y * xb.y) + (xb.z * xb.z + xb.w * xb.w);
;         const float u[8] = {xa.x * L.g[0].x, xa.y * L.g[0].y, xa.z * L.g[0].z, xa.w * L.g[0].w, xb.x * L.g[1].x, xb.y * L.g[1].y, xb.z * L.g[1].z, xb.w * L.g[1].w};
;         unsigned hb[8]; float lo[8];
; #pragma unroll
;         for (int j = 0; j < 8; ++j) { hb[j] = f2bf(u[j]); lo[j] = u[j] - __builtin_bit_cast(float, hb[j] << 16); }
;         const u32x4 hw = (u32x4){hb[0] | (hb[1] << 16), hb[2] | (hb[3] << 16), hb[4] | (hb[5] << 16), hb[6] | (hb[7] << 16)};
;         const u32x4 lw = (u32x4){pk2(lo[0], lo[1]), pk2(lo[2], lo[3]), pk2(lo[4], lo[5]), pk2(lo[6], lo[7])};
; __device__ __forceinline__ void p5_router(Frame& F) {
;     ...
;         { const int tg = wave & 1, kq = wave >> 1, fr = lane & 15, fq = lane >> 4;
;           f32x4 acc[2][5];
; #pragma unroll
;           for (int a = 0; a < 2; ++a)
; #pragma unroll
;               for (int n = 0; n < 5; ++n) acc[a][n] = (f32x4){0.f, 0.f, 0.f, 0.f};
;           float ss[2] = {0.f, 0.f};
;           const size_t roff = (size_t)(m0 + 32 * tg + fr) * D + kq * 1024 + 8 * fq;
;           const bf16_t* h0 = H + roff; const bf16_t* h1 = h0 + (size_t)16 * D;
;           const float* gp = F.g_ffn + kq * 1024 + 8 * fq;
;           const bf16_t* bh = RBH + (size_t)fr * D + kq * 1024 + 8 * fq; const bf16_t* bl = RBL + (size_t)fr * D + kq * 1024 + 8 * fq;
;           RtLoad La, Lb; rt_load(La, h0, h1, gp, 0);
; #pragma unroll 1
;           for (int ks = 0; ks < 32; ks += 2) {
;               rt_load(Lb, h0, h1, gp, (ks + 1) * 32); rt_step(La, bh, bl, acc, ss, ks * 32);
;               if (ks + 2 < 32) rt_load(La, h0, h1, gp, (ks + 2) * 32);
;               rt_step(Lb, bh, bl, acc, ss, (ks + 1) * 32); }
	s_mov_b32 s33, s94
	s_mov_b32 s94, s95
	s_mov_b32 s95, s91
	s_mov_b32 s91, s25
	s_mov_b32 s25, s33
	s_add_i32 s39, s39, 0x80
	s_and_b32 s39, s39, 0x1fff
	s_add_u32 s40, s86, s39
	s_addc_u32 s41, s87, 0
	s_add_i32 m0, s94, s98
	s_nop 0
	global_load_lds_dwordx4 v208, s[40:41]
	s_add_i32 m0, s94, s99
	s_nop 0
	global_load_lds_dwordx4 v209, s[40:41]
	s_add_i32 m0, s94, s100
	s_nop 0
	global_load_lds_dwordx4 v210, s[40:41]
	v_add_u32_e32 v214, s95, v212
	v_add_u32_e32 v215, s95, v213
	ds_read_b128 v[38:41], v215
	ds_read_b128 v[58:61], v214 offset:0
	ds_read_b128 v[62:65], v214 offset:2048
	ds_read_b128 v[66:69], v214 offset:4096
	ds_read_b128 v[70:73], v214 offset:6144
	ds_read_b128 v[74:77], v214 offset:8192
	ds_read_b128 v[100:103], v214 offset:10240
	ds_read_b128 v[104:107], v214 offset:12288
	ds_read_b128 v[108:111], v214 offset:14336
	ds_read_b128 v[112:115], v214 offset:16384
	ds_read_b128 v[116:119], v214 offset:18432
	v_mfma_f32_16x16x32_bf16 v[18:21], v[226:229], v[230:233], v[18:21]
	v_mfma_f32_16x16x32_bf16 v[22:25], v[226:229], v[234:237], v[22:25]
	v_mfma_f32_16x16x32_bf16 v[26:29], v[226:229], v[238:241], v[26:29]
	v_mfma_f32_16x16x32_bf16 v[30:33], v[226:229], v[242:245], v[30:33]
	v_mfma_f32_16x16x32_bf16 v[34:37], v[226:229], v[246:249], v[34:37]
	v_mfma_f32_16x16x32_bf16 v[42:45], v[226:229], v[226:229], v[42:45]
	v_mfma_f32_16x16x32_bf16 v[18:21], v[226:229], v[120:123], v[18:21]
	v_mfma_f32_16x16x32_bf16 v[22:25], v[226:229], v[124:127], v[22:25]
	v_mfma_f32_16x16x32_bf16 v[26:29], v[226:229], v[132:135], v[26:29]
	v_mfma_f32_16x16x32_bf16 v[30:33], v[226:229], v[136:139], v[30:33]
	v_mfma_f32_16x16x32_bf16 v[34:37], v[226:229], v[140:143], v[34:37]
	s_waitcnt vmcnt(6)
	s_waitcnt lgkmcnt(0)
	s_barrier
	s_mov_b32 s33, s94
	s_mov_b32 s94, s95
	s_mov_b32 s95, s91
	s_mov_b32 s91, s25
	s_mov_b32 s25, s33
	s_add_i32 s39, s39, 0x80
	s_and_b32 s39, s39, 0x1fff
	s_add_u32 s40, s86, s39
	s_addc_u32 s41, s87, 0
	s_add_i32 m0, s94, s98
	s_nop 0
	global_load_lds_dwordx4 v208, s[40:41]
	s_add_i32 m0, s94, s99
	s_nop 0
	global_load_lds_dwordx4 v209, s[40:41]
	s_add_i32 m0, s94, s100
	s_nop 0
	global_load_lds_dwordx4 v210, s[40:41]
	v_add_u32_e32 v214, s95, v212
	v_add_u32_e32 v215, s95, v213
	ds_read_b128 v[226:229], v215
	ds_read_b128 v[230:233], v214 offset:0
	ds_read_b128 v[234:237], v214 offset:2048
	ds_read_b128 v[238:241], v214 offset:4096
	ds_read_b128 v[242:245], v214 offset:6144
	ds_read_b128 v[246:249], v214 offset:8192
	ds_read_b128 v[120:123], v214 offset:10240
	ds_read_b128 v[124:127], v214 offset:12288
	ds_read_b128 v[132:135], v214 offset:14336
	ds_read_b128 v[136:139], v214 offset:16384
	ds_read_b128 v[140:143], v214 offset:18432
	v_mfma_f32_16x16x32_bf16 v[18:21], v[38:41], v[58:61], v[18:21]
	v_mfma_f32_16x16x32_bf16 v[22:25], v[38:41], v[62:65], v[22:25]
	v_mfma_f32_16x16x32_bf16 v[26:29], v[38:41], v[66:69], v[26:29]
	v_mfma_f32_16x16x32_bf16 v[30:33], v[38:41], v[70:73], v[30:33]
	v_mfma_f32_16x16x32_bf16 v[34:37], v[38:41], v[74:77], v[34:37]
	v_mfma_f32_16x16x32_bf16 v[42:45], v[38:41], v[38:41], v[42:45]
	v_mfma_f32_16x16x32_bf16 v[18:21], v[38:41], v[100:103], v[18:21]
	v_mfma_f32_16x16x32_bf16 v[22:25], v[38:41], v[104:107], v[22:25]
	v_mfma_f32_16x16x32_bf16 v[26:29], v[38:41], v[108:111], v[26:29]
	v_mfma_f32_16x16x32_bf16 v[30:33], v[38:41], v[112:115], v[30:33]
	v_mfma_f32_16x16x32_bf16 v[34:37], v[38:41], v[116:119], v[34:37]
	s_waitcnt vmcnt(6)
	s_waitcnt lgkmcnt(0)
	s_barrier
	s_mov_b32 s33, s94
	s_mov_b32 s94, s95
	s_mov_b32 s95, s91
	s_mov_b32 s91, s25
	s_mov_b32 s25, s33
	s_add_i32 s39, s39, 0x80
	s_and_b32 s39, s39, 0x1fff
	s_add_u32 s40, s86, s39
	s_addc_u32 s41, s87, 0
	s_add_i32 m0, s94, s98
	s_nop 0
	global_load_lds_dwordx4 v208, s[40:41]
	s_add_i32 m0, s94, s99
	s_nop 0
	global_load_lds_dwordx4 v209, s[40:41]
	s_add_i32 m0, s94, s100
	s_nop 0
	global_load_lds_dwordx4 v210, s[40:41]
	v_add_u32_e32 v214, s95, v212
	v_add_u32_e32 v215, s95, v213
	ds_read_b128 v[38:41], v215
	ds_read_b128 v[58:61], v214 offset:0
	ds_read_b128 v[62:65], v214 offset:2048
	ds_read_b128 v[66:69], v214 offset:4096
	ds_read_b128 v[70:73], v214 offset:6144
	ds_read_b128 v[74:77], v214 offset:8192
	ds_read_b128 v[100:103], v214 offset:10240
	ds_read_b128 v[104:107], v214 offset:12288
	ds_read_b128 v[108:111], v214 offset:14336
	ds_read_b128 v[112:115], v214 offset:16384
	ds_read_b128 v[116:119], v214 offset:18432
	v_mfma_f32_16x16x32_bf16 v[18:21], v[226:229], v[230:233], v[18:21]
	v_mfma_f32_16x16x32_bf16 v[22:25], v[226:229], v[234:237], v[22:25]
	v_mfma_f32_16x16x32_bf16 v[26:29], v[226:229], v[238:241], v[26:29]
	v_mfma_f32_16x16x32_bf16 v[30:33], v[226:229], v[242:245], v[30:33]
	v_mfma_f32_16x16x32_bf16 v[34:37], v[226:229], v[246:249], v[34:37]
	v_mfma_f32_16x16x32_bf16 v[42:45], v[226:229], v[226:229], v[42:45]
	v_mfma_f32_16x16x32_bf16 v[18:21], v[226:229], v[120:123], v[18:21]
	v_mfma_f32_16x16x32_bf16 v[22:25], v[226:229], v[124:127], v[22:25]
	v_mfma_f32_16x16x32_bf16 v[26:29], v[226:229], v[132:135], v[26:29]
	v_mfma_f32_16x16x32_bf16 v[30:33], v[226:229], v[136:139], v[30:33]
	v_mfma_f32_16x16x32_bf16 v[34:37], v[226:229], v[140:143], v[34:37]
	s_waitcnt vmcnt(6)
	s_waitcnt lgkmcnt(0)
	s_barrier
; __device__ __forceinline__ void rt_step(const RtLoad& L, const bf16_t* bh, const bf16_t* bl, f32x4 (&acc)[2][5], float (&ss)[2], int ko) {
;     RtW W;
; #pragma unroll
;     for (int n = 0; n < 5; ++n) { W.wh[n] = *(const bf16x8*)(bh + (size_t)n * 16 * D + ko); W.wl[n] = *(const bf16x8*)(bl + (size_t)n * 16 * D + ko); }
;     bf16x8 ahi[2], alo[2];
; #pragma unroll
;     for (int mi = 0; mi < 2; ++mi) { const u32x4 xw = L.x[mi]; const f32x4 xa = (f32x4){bflo(xw.x), bfhi(xw.x), bflo(xw.y), bfhi(xw.y)}, xb = (f32x4){bflo(xw.z), bfhi(xw.z), bflo(xw.w), bfhi(xw.w)};
;         ss[mi] += (xa.x * xa.x + xa.y * xa.y) + (xa.z * xa.z + xa.w * xa.w) + (xb.x * xb.x + xb.y * xb.y) + (xb.z * xb.z + xb.w * xb.w);
;         const float u[8] = {xa.x * L.g[0].x, xa.y * L.g[0].y, xa.z * L.g[0].z, xa.w * L.g[0].w, xb.x * L.g[1].x, xb.y * L.g[1].y, xb.z * L.g[1].z, xb.w * L.g[1].w};
;         unsigned hb[8]; float lo[8];
; #pragma unroll
;         for (int j = 0; j < 8; ++j) { hb[j] = f2bf(u[j]); lo[j] = u[j] - __builtin_bit_cast(float, hb[j] << 16); }
;         const u32x4 hw = (u32x4){hb[0] | (hb[1] << 16), hb[2] | (hb[3] << 16), hb[4] | (hb[5] << 16), hb[6] | (hb[7] << 16)};
;         const u32x4 lw = (u32x4){pk2(lo[0], lo[1]), pk2(lo[2], lo[3]), pk2(lo[4], lo[5]), pk2(lo[6], lo[7])};
; __device__ __forceinline__ void p5_router(Frame& F) {
;     ...
;         { const int tg = wave & 1, kq = wave >> 1, fr = lane & 15, fq = lane >> 4;
;           f32x4 acc[2][5];
; #pragma unroll
;           for (int a = 0; a < 2; ++a)
; #pragma unroll
;               for (int n = 0; n < 5; ++n) acc[a][n] = (f32x4){0.f, 0.f, 0.f, 0.f};
;           float ss[2] = {0.f, 0.f};
;           const size_t roff = (size_t)(m0 + 32 * tg + fr) * D + kq * 1024 + 8 * fq;
;           const bf16_t* h0 = H + roff; const bf16_t* h1 = h0 + (size_t)16 * D;
;           const float* gp = F.g_ffn + kq * 1024 + 8 * fq;
;           const bf16_t* bh = RBH + (size_t)fr * D + kq * 1024 + 8 * fq; const bf16_t* bl = RBL + (size_t)fr * D + kq * 1024 + 8 * fq;
;           RtLoad La, Lb; rt_load(La, h0, h1, gp, 0);
; #pragma unroll 1
;           for (int ks = 0; ks < 32; ks += 2) {
;               rt_load(Lb, h0, h1, gp, (ks + 1) * 32); rt_step(La, bh, bl, acc, ss, ks * 32);
;               if (ks + 2 < 32) rt_load(La, h0, h1, gp, (ks + 2) * 32);
;               rt_step(Lb, bh, bl, acc, ss, (ks + 1) * 32); }
	s_mov_b32 s33, s94
	s_mov_b32 s94, s95
	s_mov_b32 s95, s91
	s_mov_b32 s91, s25
	s_mov_b32 s25, s33
	v_add_u32_e32 v214, s95, v212
	v_add_u32_e32 v215, s95, v213
	ds_read_b128 v[226:229], v215
	ds_read_b128 v[230:233], v214 offset:0
	ds_read_b128 v[234:237], v214 offset:2048
	ds_read_b128 v[238:241], v214 offset:4096
	ds_read_b128 v[242:245], v214 offset:6144
	ds_read_b128 v[246:249], v214 offset:8192
	ds_read_b128 v[120:123], v214 offset:10240
	ds_read_b128 v[124:127], v214 offset:12288
	ds_read_b128 v[132:135], v214 offset:14336
	ds_read_b128 v[136:139], v214 offset:16384
	ds_read_b128 v[140:143], v214 offset:18432
	v_mfma_f32_16x16x32_bf16 v[18:21], v[38:41], v[58:61], v[18:21]
	v_mfma_f32_16x16x32_bf16 v[22:25], v[38:41], v[62:65], v[22:25]
	v_mfma_f32_16x16x32_bf16 v[26:29], v[38:41], v[66:69], v[26:29]
	v_mfma_f32_16x16x32_bf16 v[30:33], v[38:41], v[70:73], v[30:33]
	v_mfma_f32_16x16x32_bf16 v[34:37], v[38:41], v[74:77], v[34:37]
	v_mfma_f32_16x16x32_bf16 v[42:45], v[38:41], v[38:41], v[42:45]
	v_mfma_f32_16x16x32_bf16 v[18:21], v[38:41], v[100:103], v[18:21]
	v_mfma_f32_16x16x32_bf16 v[22:25], v[38:41], v[104:107], v[22:25]
	v_mfma_f32_16x16x32_bf16 v[26:29], v[38:41], v[108:111], v[26:29]
	v_mfma_f32_16x16x32_bf16 v[30:33], v[38:41], v[112:115], v[30:33]
	v_mfma_f32_16x16x32_bf16 v[34:37], v[38:41], v[116:119], v[34:37]
	s_waitcnt vmcnt(3)
	s_waitcnt lgkmcnt(0)
	s_barrier
	s_mov_b32 s33, s94
	s_mov_b32 s94, s95
	s_mov_b32 s95, s91
	s_mov_b32 s91, s25
	s_mov_b32 s25, s33
	v_add_u32_e32 v214, s95, v212
	v_add_u32_e32 v215, s95, v213
	ds_read_b128 v[38:41], v215
	ds_read_b128 v[58:61], v214 offset:0
	ds_read_b128 v[62:65], v214 offset:2048
	ds_read_b128 v[66:69], v214 offset:4096
	ds_read_b128 v[70:73], v214 offset:6144
	ds_read_b128 v[74:77], v214 offset:8192
	ds_read_b128 v[100:103], v214 offset:10240
	ds_read_b128 v[104:107], v214 offset:12288
	ds_read_b128 v[108:111], v214 offset:14336
	ds_read_b128 v[112:115], v214 offset:16384
	ds_read_b128 v[116:119], v214 offset:18432
	v_mfma_f32_16x16x32_bf16 v[18:21], v[226:229], v[230:233], v[18:21]
	v_mfma_f32_16x16x32_bf16 v[22:25], v[226:229], v[234:237], v[22:25]
	v_mfma_f32_16x16x32_bf16 v[26:29], v[226:229], v[238:241], v[26:29]
	v_mfma_f32_16x16x32_bf16 v[30:33], v[226:229], v[242:245], v[30:33]
	v_mfma_f32_16x16x32_bf16 v[34:37], v[226:229], v[246:249], v[34:37]
	v_mfma_f32_16x16x32_bf16 v[42:45], v[226:229], v[226:229], v[42:45]
	v_mfma_f32_16x16x32_bf16 v[18:21], v[226:229], v[120:123], v[18:21]
	v_mfma_f32_16x16x32_bf16 v[22:25], v[226:229], v[124:127], v[22:25]
	v_mfma_f32_16x16x32_bf16 v[26:29], v[226:229], v[132:135], v[26:29]
	v_mfma_f32_16x16x32_bf16 v[30:33], v[226:229], v[136:139], v[30:33]
	v_mfma_f32_16x16x32_bf16 v[34:37], v[226:229], v[140:143], v[34:37]
	s_waitcnt vmcnt(0)
	s_waitcnt lgkmcnt(0)
	s_barrier
	s_mov_b32 s33, s94
	s_mov_b32 s94, s95
	s_mov_b32 s95, s91
	s_mov_b32 s91, s25
	s_mov_b32 s25, s33
	v_add_u32_e32 v214, s95, v212
	v_add_u32_e32 v215, s95, v213
	ds_read_b128 v[226:229], v215
	ds_read_b128 v[230:233], v214 offset:0
	ds_read_b128 v[234:237], v214 offset:2048
	ds_read_b128 v[238:241], v214 offset:4096
	ds_read_b128 v[242:245], v214 offset:6144
	ds_read_b128 v[246:249], v214 offset:8192
	ds_read_b128 v[120:123], v214 offset:10240
	ds_read_b128 v[124:127], v214 offset:12288
	ds_read_b128 v[132:135], v214 offset:14336
	ds_read_b128 v[136:139], v214 offset:16384
	ds_read_b128 v[140:143], v214 offset:18432
	v_mfma_f32_16x16x32_bf16 v[18:21], v[38:41], v[58:61], v[18:21]
	v_mfma_f32_16x16x32_bf16 v[22:25], v[38:41], v[62:65], v[22:25]
	v_mfma_f32_16x16x32_bf16 v[26:29], v[38:41], v[66:69], v[26:29]
	v_mfma_f32_16x16x32_bf16 v[30:33], v[38:41], v[70:73], v[30:33]
	v_mfma_f32_16x16x32_bf16 v[34:37], v[38:41], v[74:77], v[34:37]
	v_mfma_f32_16x16x32_bf16 v[42:45], v[38:41], v[38:41], v[42:45]
	v_mfma_f32_16x16x32_bf16 v[18:21], v[38:41], v[100:103], v[18:21]
	v_mfma_f32_16x16x32_bf16 v[22:25], v[38:41], v[104:107], v[22:25]
	v_mfma_f32_16x16x32_bf16 v[26:29], v[38:41], v[108:111], v[26:29]
	v_mfma_f32_16x16x32_bf16 v[30:33], v[38:41], v[112:115], v[30:33]
	v_mfma_f32_16x16x32_bf16 v[34:37], v[38:41], v[116:119], v[34:37]
	s_waitcnt lgkmcnt(0)
	s_barrier
	s_mov_b32 s33, s94
	s_mov_b32 s94, s95
	s_mov_b32 s95, s91
	s_mov_b32 s91, s25
	s_mov_b32 s25, s33
	v_mfma_f32_16x16x32_bf16 v[18:21], v[226:229], v[230:233], v[18:21]
	v_mfma_f32_16x16x32_bf16 v[22:25], v[226:229], v[234:237], v[22:25]
	v_mfma_f32_16x16x32_bf16 v[26:29], v[226:229], v[238:241], v[26:29]
	v_mfma_f32_16x16x32_bf16 v[30:33], v[226:229], v[242:245], v[30:33]
	v_mfma_f32_16x16x32_bf16 v[34:37], v[226:229], v[246:249], v[34:37]
	v_mfma_f32_16x16x32_bf16 v[42:45], v[226:229], v[226:229], v[42:45]
	v_mfma_f32_16x16x32_bf16 v[18:21], v[226:229], v[120:123], v[18:21]
	v_mfma_f32_16x16x32_bf16 v[22:25], v[226:229], v[124:127], v[22:25]
	v_mfma_f32_16x16x32_bf16 v[26:29], v[226:229], v[132:135], v[26:29]
	v_mfma_f32_16x16x32_bf16 v[30:33], v[226:229], v[136:139], v[30:33]
	v_mfma_f32_16x16x32_bf16 v[34:37], v[226:229], v[140:143], v[34:37]
; __device__ __forceinline__ void p5_router(Frame& F) {
;     ...
;           for (int mi = 0; mi < 2; ++mi) { float s = ss[mi]; s += __shfl_xor(s, 16); s += __shfl_xor(s, 32); if (fq == 0) ssp[kq * 64 + 32 * tg + 16 * mi + fr] = s;
; #pragma unroll
;               for (int n = 0; n < 5; ++n)
; #pragma unroll
;                   for (int i = 0; i < 4; ++i) part[(kq * 64 + 32 * tg + 16 * mi + 4 * fq + i) * 80 + 16 * n + fr] = acc[mi][n][i]; } }
;         __syncthreads();
;         if (F.tid < 64) { const float s = (ssp[F.tid] + ssp[64 + F.tid]) + (ssp[128 + F.tid] + ssp[192 + F.tid]); const float r = 1.0f / sqrtf(s * (1.f / D) + RMS_EPS); rs[F.tid] = r; }
.Lrt_out:
	s_nop 7
	s_nop 7
	s_lshl_b32 s24, s89, 6
	s_lshl_b32 s33, s88, 4
	s_add_i32 s24, s24, s33
	s_mul_i32 s33, s24, 320
	v_mul_u32_u24_e32 v217, 0x500, v171
	v_lshl_add_u32 v217, v170, 2, v217
	v_add_u32_e32 v217, s33, v217
	ds_write_b32 v217, v18 offset:0
	ds_write_b32 v217, v19 offset:320
	ds_write_b32 v217, v20 offset:640
	ds_write_b32 v217, v21 offset:960
	ds_write_b32 v217, v22 offset:64
	ds_write_b32 v217, v23 offset:384
	ds_write_b32 v217, v24 offset:704
	ds_write_b32 v217, v25 offset:1024
	ds_write_b32 v217, v26 offset:128
	ds_write_b32 v217, v27 offset:448
	ds_write_b32 v217, v28 offset:768
	ds_write_b32 v217, v29 offset:1088
	ds_write_b32 v217, v30 offset:192
	ds_write_b32 v217, v31 offset:512
	ds_write_b32 v217, v32 offset:832
	ds_write_b32 v217, v33 offset:1152
	ds_write_b32 v217, v34 offset:256
	ds_write_b32 v217, v35 offset:576
	ds_write_b32 v217, v36 offset:896
	ds_write_b32 v217, v37 offset:1216
	v_mov_b32_e32 v218, 0
	v_mov_b32_e32 v219, 0
	v_mov_b32_e32 v220, 0
	v_mov_b32_e32 v221, 0
	v_lshlrev_b32_e32 v222, 4, v0
	v_add_u32_e32 v222, 0xa000, v222
	ds_write_b128 v222, v[218:221] offset:0
	ds_write_b128 v222, v[218:221] offset:8192
	ds_write_b128 v222, v[218:221] offset:16384
	ds_write_b128 v222, v[218:221] offset:24576
	ds_write_b128 v222, v[218:221] offset:32768
	v_and_b32_e32 v222, 3, v170
	v_mov_b32_e32 v223, v42
	v_cmp_eq_u32_e32 vcc, 1, v222
	v_cndmask_b32_e32 v223, v223, v43, vcc
	v_cmp_eq_u32_e32 vcc, 2, v222
	v_cndmask_b32_e32 v223, v223, v44, vcc
	v_cmp_eq_u32_e32 vcc, 3, v222
	v_cndmask_b32_e32 v223, v223, v45, vcc
	s_lshl_b32 s24, s24, 2
	s_add_i32 s24, s24, 0x19000
	v_lshl_add_u32 v217, v170, 2, s24
	v_lshrrev_b32_e32 v222, 2, v170
	v_cmp_eq_u32_e32 vcc, v222, v171
	s_and_saveexec_b64 s[98:99], vcc
	ds_write_b32 v217, v223
	s_or_b64 exec, exec, s[98:99]
	v_cmp_gt_u32_e32 vcc, 0x80, v0
	v_lshlrev_b32_e32 v222, 2, v0
	v_add_u32_e32 v222, 0x19200, v222
	s_and_saveexec_b64 s[98:99], vcc
	ds_write_b32 v222, v218
	s_or_b64 exec, exec, s[98:99]
	s_waitcnt lgkmcnt(0)
	s_barrier
	s_and_saveexec_b64 s[8:9], s[4:5]
	s_cbranch_execz .LBB0_616
	ds_read2st64_b32 v[2:3], v147 offset1:1
	ds_read2st64_b32 v[4:5], v147 offset0:2 offset1:3
	s_waitcnt lgkmcnt(1)
	v_mov_b32_e32 v6, v2
	s_waitcnt lgkmcnt(0)
	v_mov_b32_e32 v7, v4
	v_mov_b32_e32 v4, v3
	v_pk_add_f32 v[2:3], v[6:7], v[4:5]
	s_nop 0
	v_add_f32_e32 v2, v2, v3
	v_fmamk_f32 v2, v2, 0x39800000, v151
	v_mul_f32_e32 v3, 0x4f800000, v2
	v_cmp_gt_f32_e32 vcc, s57, v2
	s_nop 1
	v_cndmask_b32_e32 v2, v2, v3, vcc
	v_sqrt_f32_e32 v3, v2
	s_nop 0
	v_add_u32_e32 v4, -1, v3
	v_add_u32_e32 v5, 1, v3
	v_fma_f32 v6, -v4, v3, v2
	v_fma_f32 v7, -v5, v3, v2
	v_cmp_ge_f32_e64 s[0:1], 0, v6
	s_nop 1
	v_cndmask_b32_e64 v3, v3, v4, s[0:1]
	v_cmp_lt_f32_e64 s[0:1], 0, v7
	s_nop 1
	v_cndmask_b32_e64 v3, v3, v5, s[0:1]
	v_mul_f32_e32 v4, 0x37800000, v3
	v_cndmask_b32_e32 v3, v3, v4, vcc
	v_cmp_class_f32_e32 vcc, v2, v152
	s_nop 1
	v_cndmask_b32_e32 v2, v3, v2, vcc
	v_div_scale_f32 v3, s[0:1], v2, v2, 1.0
	v_rcp_f32_e32 v4, v3
	s_nop 0
	v_fma_f32 v5, -v3, v4, 1.0
	v_fmac_f32_e32 v4, v5, v4
	v_div_scale_f32 v5, vcc, 1.0, v2, 1.0
	v_mul_f32_e32 v6, v5, v4
	v_fma_f32 v7, -v3, v6, v5
	v_fmac_f32_e32 v6, v7, v4
	v_fma_f32 v3, -v3, v6, v5
	v_div_fmas_f32 v3, v3, v4, v6
	v_div_fixup_f32 v2, v3, v2, 1.0
	ds_write_b32 v148, v2
